# stack on v102: GEMM back-edge rotation + norm1 top-of-row wait removed + conv LayerNorm gain/bias loads hoisted out of the token loop
# speedup vs baseline: 1.0049x; 1.0049x over previous
.LBB0_491:
	s_or_b64 exec, exec, s[0:1]
	s_waitcnt lgkmcnt(0)
	s_barrier
	ds_read2st64_b32 v[118:119], v104 offset1:4
	ds_read2st64_b32 v[120:121], v104 offset0:8 offset1:12
	ds_read2st64_b32 v[70:71], v104 offset0:16 offset1:20
	ds_read2st64_b32 v[68:69], v104 offset0:24 offset1:28
	ds_read2st64_b32 v[66:67], v104 offset0:32 offset1:36
	ds_read2st64_b32 v[64:65], v104 offset0:40 offset1:44
	ds_read2st64_b32 v[62:63], v104 offset0:48 offset1:52
	s_waitcnt vmcnt(0)
	ds_read2st64_b32 v[46:47], v104 offset0:56 offset1:60
	ds_read2st64_b32 v[44:45], v104 offset0:64 offset1:68
	ds_read2st64_b32 v[42:43], v104 offset0:72 offset1:76
	ds_read2st64_b32 v[40:41], v104 offset0:80 offset1:84
	ds_read2st64_b32 v[38:39], v104 offset0:88 offset1:92
	ds_read2st64_b32 v[36:37], v104 offset0:96 offset1:100
	ds_read2st64_b32 v[34:35], v104 offset0:104 offset1:108
	ds_read2st64_b32 v[32:33], v104 offset0:112 offset1:116
	ds_read2st64_b32 v[30:31], v104 offset0:120 offset1:124
	ds_read2st64_b32 v[28:29], v104 offset0:128 offset1:132
	ds_read2st64_b32 v[26:27], v104 offset0:136 offset1:140
	ds_read2st64_b32 v[24:25], v104 offset0:144 offset1:148
	ds_read2st64_b32 v[22:23], v104 offset0:152 offset1:156
	ds_read2st64_b32 v[20:21], v104 offset0:160 offset1:164
	ds_read2st64_b32 v[18:19], v104 offset0:168 offset1:172
	ds_read2st64_b32 v[16:17], v104 offset0:176 offset1:180
	ds_read2st64_b32 v[14:15], v104 offset0:184 offset1:188
	ds_read2st64_b32 v[12:13], v104 offset0:192 offset1:196
	ds_read2st64_b32 v[10:11], v104 offset0:200 offset1:204
	ds_read2st64_b32 v[8:9], v104 offset0:208 offset1:212
	ds_read2st64_b32 v[6:7], v104 offset0:216 offset1:220
	ds_read2st64_b32 v[4:5], v104 offset0:224 offset1:228
	ds_read2st64_b32 v[2:3], v104 offset0:232 offset1:236
	ds_read2st64_b32 v[0:1], v104 offset0:240 offset1:244
	s_waitcnt lgkmcnt(14)
	v_fma_f32 v117, v51, v118, v103
	v_fmac_f32_e32 v117, v72, v119
	v_fma_f32 v118, v51, v119, v103
	v_fmac_f32_e32 v117, v73, v120
	v_fmac_f32_e32 v118, v72, v120
	v_fma_f32 v119, v51, v120, v103
	v_fmac_f32_e32 v117, v74, v121
	v_fmac_f32_e32 v118, v73, v121
	v_fmac_f32_e32 v119, v72, v121
	v_fma_f32 v120, v51, v121, v103
	v_fmac_f32_e32 v117, v75, v70
	v_fmac_f32_e32 v118, v74, v70
	v_fmac_f32_e32 v119, v73, v70
	v_fmac_f32_e32 v120, v72, v70
	v_fma_f32 v70, v51, v70, v103
	v_fmac_f32_e32 v117, v76, v71
	v_fmac_f32_e32 v118, v75, v71
	v_fmac_f32_e32 v119, v74, v71
	v_fmac_f32_e32 v120, v73, v71
	v_fmac_f32_e32 v70, v72, v71
	v_fma_f32 v71, v51, v71, v103
	v_fmac_f32_e32 v117, v77, v68
	v_fmac_f32_e32 v118, v76, v68
	v_fmac_f32_e32 v119, v75, v68
	v_fmac_f32_e32 v120, v74, v68
	v_fmac_f32_e32 v70, v73, v68
	v_fmac_f32_e32 v71, v72, v68
	v_fma_f32 v68, v51, v68, v103
	v_fmac_f32_e32 v117, v78, v69
	v_fmac_f32_e32 v118, v77, v69
	v_fmac_f32_e32 v119, v76, v69
	v_fmac_f32_e32 v120, v75, v69
	v_fmac_f32_e32 v70, v74, v69
	v_fmac_f32_e32 v71, v73, v69
	v_fmac_f32_e32 v68, v72, v69
	v_fma_f32 v69, v51, v69, v103
	v_fmac_f32_e32 v117, v79, v66
	v_fmac_f32_e32 v118, v78, v66
	v_fmac_f32_e32 v119, v77, v66
	v_fmac_f32_e32 v120, v76, v66
	v_fmac_f32_e32 v70, v75, v66
	v_fmac_f32_e32 v71, v74, v66
	v_fmac_f32_e32 v68, v73, v66
	v_fmac_f32_e32 v69, v72, v66
	v_fma_f32 v66, v51, v66, v103
	v_fmac_f32_e32 v117, v80, v67
	v_fmac_f32_e32 v118, v79, v67
	v_fmac_f32_e32 v119, v78, v67
	v_fmac_f32_e32 v120, v77, v67
	v_fmac_f32_e32 v70, v76, v67
	v_fmac_f32_e32 v71, v75, v67
	v_fmac_f32_e32 v68, v74, v67
	v_fmac_f32_e32 v69, v73, v67
	v_fmac_f32_e32 v66, v72, v67
	v_fma_f32 v67, v51, v67, v103
	v_fmac_f32_e32 v117, v81, v64
	v_fmac_f32_e32 v118, v80, v64
	v_fmac_f32_e32 v119, v79, v64
	v_fmac_f32_e32 v120, v78, v64
	v_fmac_f32_e32 v70, v77, v64
	v_fmac_f32_e32 v71, v76, v64
	v_fmac_f32_e32 v68, v75, v64
	v_fmac_f32_e32 v69, v74, v64
	v_fmac_f32_e32 v66, v73, v64
	v_fmac_f32_e32 v67, v72, v64
	v_fma_f32 v64, v51, v64, v103
	v_fmac_f32_e32 v117, v82, v65
	v_fmac_f32_e32 v118, v81, v65
	v_fmac_f32_e32 v119, v80, v65
	v_fmac_f32_e32 v120, v79, v65
	v_fmac_f32_e32 v70, v78, v65
	v_fmac_f32_e32 v71, v77, v65
	v_fmac_f32_e32 v68, v76, v65
	v_fmac_f32_e32 v69, v75, v65
	v_fmac_f32_e32 v66, v74, v65
	v_fmac_f32_e32 v67, v73, v65
	v_fmac_f32_e32 v64, v72, v65
	v_fma_f32 v65, v51, v65, v103
	v_fmac_f32_e32 v117, v83, v62
	v_fmac_f32_e32 v118, v82, v62
	v_fmac_f32_e32 v119, v81, v62
	v_fmac_f32_e32 v120, v80, v62
	v_fmac_f32_e32 v70, v79, v62
	v_fmac_f32_e32 v71, v78, v62
	v_fmac_f32_e32 v68, v77, v62
	v_fmac_f32_e32 v69, v76, v62
	v_fmac_f32_e32 v66, v75, v62
	v_fmac_f32_e32 v67, v74, v62
	v_fmac_f32_e32 v64, v73, v62
	v_fmac_f32_e32 v65, v72, v62
	v_fma_f32 v62, v51, v62, v103
	v_fmac_f32_e32 v117, v84, v63
	v_fmac_f32_e32 v118, v83, v63
	v_fmac_f32_e32 v119, v82, v63
	v_fmac_f32_e32 v120, v81, v63
	v_fmac_f32_e32 v70, v80, v63
	v_fmac_f32_e32 v71, v79, v63
	v_fmac_f32_e32 v68, v78, v63
	v_fmac_f32_e32 v69, v77, v63
	v_fmac_f32_e32 v66, v76, v63
	v_fmac_f32_e32 v67, v75, v63
	v_fmac_f32_e32 v64, v74, v63
	v_fmac_f32_e32 v65, v73, v63
	v_fmac_f32_e32 v62, v72, v63
	v_fma_f32 v63, v51, v63, v103
	v_fmac_f32_e32 v117, v85, v46
	v_fmac_f32_e32 v118, v84, v46
	v_fmac_f32_e32 v119, v83, v46
	v_fmac_f32_e32 v120, v82, v46
	v_fmac_f32_e32 v70, v81, v46
	v_fmac_f32_e32 v71, v80, v46
	v_fmac_f32_e32 v68, v79, v46
	v_fmac_f32_e32 v69, v78, v46
	v_fmac_f32_e32 v66, v77, v46
	v_fmac_f32_e32 v67, v76, v46
	v_fmac_f32_e32 v64, v75, v46
	v_fmac_f32_e32 v65, v74, v46
	v_fmac_f32_e32 v62, v73, v46
	v_fmac_f32_e32 v63, v72, v46
	v_fma_f32 v46, v51, v46, v103
	v_fmac_f32_e32 v117, v86, v47
	v_fmac_f32_e32 v118, v85, v47
	v_fmac_f32_e32 v119, v84, v47
	v_fmac_f32_e32 v120, v83, v47
	v_fmac_f32_e32 v70, v82, v47
	v_fmac_f32_e32 v71, v81, v47
	v_fmac_f32_e32 v68, v80, v47
	v_fmac_f32_e32 v69, v79, v47
	v_fmac_f32_e32 v66, v78, v47
	v_fmac_f32_e32 v67, v77, v47
	v_fmac_f32_e32 v64, v76, v47
	v_fmac_f32_e32 v65, v75, v47
	v_fmac_f32_e32 v62, v74, v47
	v_fmac_f32_e32 v63, v73, v47
	v_fmac_f32_e32 v46, v72, v47
	v_fma_f32 v47, v51, v47, v103
	v_fmac_f32_e32 v117, v87, v44
	v_fmac_f32_e32 v118, v86, v44
	v_fmac_f32_e32 v119, v85, v44
	v_fmac_f32_e32 v120, v84, v44
	v_fmac_f32_e32 v70, v83, v44
	v_fmac_f32_e32 v71, v82, v44
	v_fmac_f32_e32 v68, v81, v44
	v_fmac_f32_e32 v69, v80, v44
	v_fmac_f32_e32 v66, v79, v44
	v_fmac_f32_e32 v67, v78, v44
	v_fmac_f32_e32 v64, v77, v44
	v_fmac_f32_e32 v65, v76, v44
	v_fmac_f32_e32 v62, v75, v44
	v_fmac_f32_e32 v63, v74, v44
	v_fmac_f32_e32 v46, v73, v44
	v_fmac_f32_e32 v47, v72, v44
	v_fma_f32 v44, v51, v44, v103
	v_fmac_f32_e32 v117, v88, v45
	v_fmac_f32_e32 v118, v87, v45
	v_fmac_f32_e32 v119, v86, v45
	v_fmac_f32_e32 v120, v85, v45
	v_fmac_f32_e32 v70, v84, v45
	v_fmac_f32_e32 v71, v83, v45
	v_fmac_f32_e32 v68, v82, v45
	v_fmac_f32_e32 v69, v81, v45
	v_fmac_f32_e32 v66, v80, v45
	v_fmac_f32_e32 v67, v79, v45
	v_fmac_f32_e32 v64, v78, v45
	v_fmac_f32_e32 v65, v77, v45
	v_fmac_f32_e32 v62, v76, v45
	v_fmac_f32_e32 v63, v75, v45
	v_fmac_f32_e32 v46, v74, v45
	v_fmac_f32_e32 v47, v73, v45
	v_fmac_f32_e32 v44, v72, v45
	v_fma_f32 v45, v51, v45, v103
	v_fmac_f32_e32 v117, v89, v42
	v_fmac_f32_e32 v118, v88, v42
	v_fmac_f32_e32 v119, v87, v42
	v_fmac_f32_e32 v120, v86, v42
	v_fmac_f32_e32 v70, v85, v42
	v_fmac_f32_e32 v71, v84, v42
	v_fmac_f32_e32 v68, v83, v42
	v_fmac_f32_e32 v69, v82, v42
	v_fmac_f32_e32 v66, v81, v42
	v_fmac_f32_e32 v67, v80, v42
	v_fmac_f32_e32 v64, v79, v42
	v_fmac_f32_e32 v65, v78, v42
	v_fmac_f32_e32 v62, v77, v42
	v_fmac_f32_e32 v63, v76, v42
	v_fmac_f32_e32 v46, v75, v42
	v_fmac_f32_e32 v47, v74, v42
	v_fmac_f32_e32 v44, v73, v42
	v_fmac_f32_e32 v45, v72, v42
	v_fma_f32 v42, v51, v42, v103
	v_fmac_f32_e32 v117, v90, v43
	v_fmac_f32_e32 v118, v89, v43
	v_fmac_f32_e32 v119, v88, v43
	v_fmac_f32_e32 v120, v87, v43
	v_fmac_f32_e32 v70, v86, v43
	v_fmac_f32_e32 v71, v85, v43
	v_fmac_f32_e32 v68, v84, v43
	v_fmac_f32_e32 v69, v83, v43
	v_fmac_f32_e32 v66, v82, v43
	v_fmac_f32_e32 v67, v81, v43
	v_fmac_f32_e32 v64, v80, v43
	v_fmac_f32_e32 v65, v79, v43
	v_fmac_f32_e32 v62, v78, v43
	v_fmac_f32_e32 v63, v77, v43
	v_fmac_f32_e32 v46, v76, v43
	v_fmac_f32_e32 v47, v75, v43
	v_fmac_f32_e32 v44, v74, v43
	v_fmac_f32_e32 v45, v73, v43
	v_fmac_f32_e32 v42, v72, v43
	v_fma_f32 v43, v51, v43, v103
	v_fmac_f32_e32 v117, v91, v40
	v_fmac_f32_e32 v118, v90, v40
	v_fmac_f32_e32 v119, v89, v40
	v_fmac_f32_e32 v120, v88, v40
	v_fmac_f32_e32 v70, v87, v40
	v_fmac_f32_e32 v71, v86, v40
	v_fmac_f32_e32 v68, v85, v40
	v_fmac_f32_e32 v69, v84, v40
	v_fmac_f32_e32 v66, v83, v40
	v_fmac_f32_e32 v67, v82, v40
	v_fmac_f32_e32 v64, v81, v40
	v_fmac_f32_e32 v65, v80, v40
	v_fmac_f32_e32 v62, v79, v40
	v_fmac_f32_e32 v63, v78, v40
	v_fmac_f32_e32 v46, v77, v40
	v_fmac_f32_e32 v47, v76, v40
	v_fmac_f32_e32 v44, v75, v40
	v_fmac_f32_e32 v45, v74, v40
	v_fmac_f32_e32 v42, v73, v40
	v_fmac_f32_e32 v43, v72, v40
	v_fma_f32 v40, v51, v40, v103
	v_fmac_f32_e32 v117, v92, v41
	v_fmac_f32_e32 v118, v91, v41
	v_fmac_f32_e32 v119, v90, v41
	v_fmac_f32_e32 v120, v89, v41
	v_fmac_f32_e32 v70, v88, v41
	v_fmac_f32_e32 v71, v87, v41
	v_fmac_f32_e32 v68, v86, v41
	v_fmac_f32_e32 v69, v85, v41
	v_fmac_f32_e32 v66, v84, v41
	v_fmac_f32_e32 v67, v83, v41
	v_fmac_f32_e32 v64, v82, v41
	v_fmac_f32_e32 v65, v81, v41
	v_fmac_f32_e32 v62, v80, v41
	v_fmac_f32_e32 v63, v79, v41
	v_fmac_f32_e32 v46, v78, v41
	v_fmac_f32_e32 v47, v77, v41
	v_fmac_f32_e32 v44, v76, v41
	v_fmac_f32_e32 v45, v75, v41
	v_fmac_f32_e32 v42, v74, v41
	v_fmac_f32_e32 v43, v73, v41
	v_fmac_f32_e32 v40, v72, v41
	v_fma_f32 v41, v51, v41, v103
	v_fmac_f32_e32 v117, v93, v38
	v_fmac_f32_e32 v118, v92, v38
	v_fmac_f32_e32 v119, v91, v38
	v_fmac_f32_e32 v120, v90, v38
	v_fmac_f32_e32 v70, v89, v38
	v_fmac_f32_e32 v71, v88, v38
	v_fmac_f32_e32 v68, v87, v38
	v_fmac_f32_e32 v69, v86, v38
	v_fmac_f32_e32 v66, v85, v38
	v_fmac_f32_e32 v67, v84, v38
	v_fmac_f32_e32 v64, v83, v38
	v_fmac_f32_e32 v65, v82, v38
	v_fmac_f32_e32 v62, v81, v38
	v_fmac_f32_e32 v63, v80, v38
	v_fmac_f32_e32 v46, v79, v38
	v_fmac_f32_e32 v47, v78, v38
	v_fmac_f32_e32 v44, v77, v38
	v_fmac_f32_e32 v45, v76, v38
	v_fmac_f32_e32 v42, v75, v38
	v_fmac_f32_e32 v43, v74, v38
	v_fmac_f32_e32 v40, v73, v38
	v_fmac_f32_e32 v41, v72, v38
	v_fma_f32 v38, v51, v38, v103
	v_fmac_f32_e32 v117, v94, v39
	v_fmac_f32_e32 v118, v93, v39
	v_fmac_f32_e32 v119, v92, v39
	v_fmac_f32_e32 v120, v91, v39
	v_fmac_f32_e32 v70, v90, v39
	v_fmac_f32_e32 v71, v89, v39
	v_fmac_f32_e32 v68, v88, v39
	v_fmac_f32_e32 v69, v87, v39
	v_fmac_f32_e32 v66, v86, v39
	v_fmac_f32_e32 v67, v85, v39
	v_fmac_f32_e32 v64, v84, v39
	v_fmac_f32_e32 v65, v83, v39
	v_fmac_f32_e32 v62, v82, v39
	v_fmac_f32_e32 v63, v81, v39
	v_fmac_f32_e32 v46, v80, v39
	v_fmac_f32_e32 v47, v79, v39
	v_fmac_f32_e32 v44, v78, v39
	v_fmac_f32_e32 v45, v77, v39
	v_fmac_f32_e32 v42, v76, v39
	v_fmac_f32_e32 v43, v75, v39
	v_fmac_f32_e32 v40, v74, v39
	v_fmac_f32_e32 v41, v73, v39
	v_fmac_f32_e32 v38, v72, v39
	v_fma_f32 v39, v51, v39, v103
	v_fmac_f32_e32 v117, v95, v36
	v_fmac_f32_e32 v118, v94, v36
	v_fmac_f32_e32 v119, v93, v36
	v_fmac_f32_e32 v120, v92, v36
	v_fmac_f32_e32 v70, v91, v36
	v_fmac_f32_e32 v71, v90, v36
	v_fmac_f32_e32 v68, v89, v36
	v_fmac_f32_e32 v69, v88, v36
	v_fmac_f32_e32 v66, v87, v36
	v_fmac_f32_e32 v67, v86, v36
	v_fmac_f32_e32 v64, v85, v36
	v_fmac_f32_e32 v65, v84, v36
	v_fmac_f32_e32 v62, v83, v36
	v_fmac_f32_e32 v63, v82, v36
	v_fmac_f32_e32 v46, v81, v36
	v_fmac_f32_e32 v47, v80, v36
	v_fmac_f32_e32 v44, v79, v36
	v_fmac_f32_e32 v45, v78, v36
	v_fmac_f32_e32 v42, v77, v36
	v_fmac_f32_e32 v43, v76, v36
	v_fmac_f32_e32 v40, v75, v36
	v_fmac_f32_e32 v41, v74, v36
	v_fmac_f32_e32 v38, v73, v36
	v_fmac_f32_e32 v39, v72, v36
	v_fma_f32 v36, v51, v36, v103
	v_fmac_f32_e32 v117, v96, v37
	v_fmac_f32_e32 v118, v95, v37
	v_fmac_f32_e32 v119, v94, v37
	v_fmac_f32_e32 v120, v93, v37
	v_fmac_f32_e32 v70, v92, v37
	v_fmac_f32_e32 v71, v91, v37
	v_fmac_f32_e32 v68, v90, v37
	v_fmac_f32_e32 v69, v89, v37
	v_fmac_f32_e32 v66, v88, v37
	v_fmac_f32_e32 v67, v87, v37
	v_fmac_f32_e32 v64, v86, v37
	v_fmac_f32_e32 v65, v85, v37
	v_fmac_f32_e32 v62, v84, v37
	v_fmac_f32_e32 v63, v83, v37
	v_fmac_f32_e32 v46, v82, v37
	v_fmac_f32_e32 v47, v81, v37
	v_fmac_f32_e32 v44, v80, v37
	v_fmac_f32_e32 v45, v79, v37
	v_fmac_f32_e32 v42, v78, v37
	v_fmac_f32_e32 v43, v77, v37
	v_fmac_f32_e32 v40, v76, v37
	v_fmac_f32_e32 v41, v75, v37
	v_fmac_f32_e32 v38, v74, v37
	v_fmac_f32_e32 v39, v73, v37
	v_fmac_f32_e32 v36, v72, v37
	v_fma_f32 v37, v51, v37, v103
	v_fmac_f32_e32 v117, v97, v34
	v_fmac_f32_e32 v118, v96, v34
	v_fmac_f32_e32 v119, v95, v34
	v_fmac_f32_e32 v120, v94, v34
	v_fmac_f32_e32 v70, v93, v34
	v_fmac_f32_e32 v71, v92, v34
	v_fmac_f32_e32 v68, v91, v34
	v_fmac_f32_e32 v69, v90, v34
	v_fmac_f32_e32 v66, v89, v34
	v_fmac_f32_e32 v67, v88, v34
	v_fmac_f32_e32 v64, v87, v34
	v_fmac_f32_e32 v65, v86, v34
	v_fmac_f32_e32 v62, v85, v34
	v_fmac_f32_e32 v63, v84, v34
	v_fmac_f32_e32 v46, v83, v34
	v_fmac_f32_e32 v47, v82, v34
	v_fmac_f32_e32 v44, v81, v34
	v_fmac_f32_e32 v45, v80, v34
	v_fmac_f32_e32 v42, v79, v34
	v_fmac_f32_e32 v43, v78, v34
	v_fmac_f32_e32 v40, v77, v34
	v_fmac_f32_e32 v41, v76, v34
	v_fmac_f32_e32 v38, v75, v34
	v_fmac_f32_e32 v39, v74, v34
	v_fmac_f32_e32 v36, v73, v34
	v_fmac_f32_e32 v37, v72, v34
	v_fma_f32 v34, v51, v34, v103
	v_fmac_f32_e32 v117, v98, v35
	v_fmac_f32_e32 v118, v97, v35
	v_fmac_f32_e32 v119, v96, v35
	v_fmac_f32_e32 v120, v95, v35
	v_fmac_f32_e32 v70, v94, v35
	v_fmac_f32_e32 v71, v93, v35
	v_fmac_f32_e32 v68, v92, v35
	v_fmac_f32_e32 v69, v91, v35
	v_fmac_f32_e32 v66, v90, v35
	v_fmac_f32_e32 v67, v89, v35
	v_fmac_f32_e32 v64, v88, v35
	v_fmac_f32_e32 v65, v87, v35
	v_fmac_f32_e32 v62, v86, v35
	v_fmac_f32_e32 v63, v85, v35
	v_fmac_f32_e32 v46, v84, v35
	v_fmac_f32_e32 v47, v83, v35
	v_fmac_f32_e32 v44, v82, v35
	v_fmac_f32_e32 v45, v81, v35
	v_fmac_f32_e32 v42, v80, v35
	v_fmac_f32_e32 v43, v79, v35
	v_fmac_f32_e32 v40, v78, v35
	v_fmac_f32_e32 v41, v77, v35
	v_fmac_f32_e32 v38, v76, v35
	v_fmac_f32_e32 v39, v75, v35
	v_fmac_f32_e32 v36, v74, v35
	v_fmac_f32_e32 v37, v73, v35
	v_fmac_f32_e32 v34, v72, v35
	v_fma_f32 v35, v51, v35, v103
	v_fmac_f32_e32 v117, v99, v32
	v_fmac_f32_e32 v118, v98, v32
	v_fmac_f32_e32 v119, v97, v32
	v_fmac_f32_e32 v120, v96, v32
	v_fmac_f32_e32 v70, v95, v32
	v_fmac_f32_e32 v71, v94, v32
	v_fmac_f32_e32 v68, v93, v32
	v_fmac_f32_e32 v69, v92, v32
	v_fmac_f32_e32 v66, v91, v32
	v_fmac_f32_e32 v67, v90, v32
	v_fmac_f32_e32 v64, v89, v32
	v_fmac_f32_e32 v65, v88, v32
	v_fmac_f32_e32 v62, v87, v32
	v_fmac_f32_e32 v63, v86, v32
	v_fmac_f32_e32 v46, v85, v32
	v_fmac_f32_e32 v47, v84, v32
	v_fmac_f32_e32 v44, v83, v32
	v_fmac_f32_e32 v45, v82, v32
	v_fmac_f32_e32 v42, v81, v32
	v_fmac_f32_e32 v43, v80, v32
	v_fmac_f32_e32 v40, v79, v32
	v_fmac_f32_e32 v41, v78, v32
	v_fmac_f32_e32 v38, v77, v32
	v_fmac_f32_e32 v39, v76, v32
	v_fmac_f32_e32 v36, v75, v32
	v_fmac_f32_e32 v37, v74, v32
	v_fmac_f32_e32 v34, v73, v32
	v_fmac_f32_e32 v35, v72, v32
	v_fma_f32 v32, v51, v32, v103
	v_fmac_f32_e32 v117, v101, v33
	v_fmac_f32_e32 v118, v99, v33
	v_fmac_f32_e32 v119, v98, v33
	v_fmac_f32_e32 v120, v97, v33
	v_fmac_f32_e32 v70, v96, v33
	v_fmac_f32_e32 v71, v95, v33
	v_fmac_f32_e32 v68, v94, v33
	v_fmac_f32_e32 v69, v93, v33
	v_fmac_f32_e32 v66, v92, v33
	v_fmac_f32_e32 v67, v91, v33
	v_fmac_f32_e32 v64, v90, v33
	v_fmac_f32_e32 v65, v89, v33
	v_fmac_f32_e32 v62, v88, v33
	v_fmac_f32_e32 v63, v87, v33
	v_fmac_f32_e32 v46, v86, v33
	v_fmac_f32_e32 v47, v85, v33
	v_fmac_f32_e32 v44, v84, v33
	v_fmac_f32_e32 v45, v83, v33
	v_fmac_f32_e32 v42, v82, v33
	v_fmac_f32_e32 v43, v81, v33
	v_fmac_f32_e32 v40, v80, v33
	v_fmac_f32_e32 v41, v79, v33
	v_fmac_f32_e32 v38, v78, v33
	v_fmac_f32_e32 v39, v77, v33
	v_fmac_f32_e32 v36, v76, v33
	v_fmac_f32_e32 v37, v75, v33
	v_fmac_f32_e32 v34, v74, v33
	v_fmac_f32_e32 v35, v73, v33
	v_fmac_f32_e32 v32, v72, v33
	v_fma_f32 v33, v51, v33, v103
	v_fmac_f32_e32 v117, v102, v30
	v_fmac_f32_e32 v118, v101, v30
	v_fmac_f32_e32 v119, v99, v30
	v_fmac_f32_e32 v120, v98, v30
	v_fmac_f32_e32 v70, v97, v30
	v_fmac_f32_e32 v71, v96, v30
	v_fmac_f32_e32 v68, v95, v30
	v_fmac_f32_e32 v69, v94, v30
	v_fmac_f32_e32 v66, v93, v30
	v_fmac_f32_e32 v67, v92, v30
	v_fmac_f32_e32 v64, v91, v30
	v_fmac_f32_e32 v65, v90, v30
	v_fmac_f32_e32 v62, v89, v30
	v_fmac_f32_e32 v63, v88, v30
	v_fmac_f32_e32 v46, v87, v30
	v_fmac_f32_e32 v47, v86, v30
	v_fmac_f32_e32 v44, v85, v30
	v_fmac_f32_e32 v45, v84, v30
	v_fmac_f32_e32 v42, v83, v30
	v_fmac_f32_e32 v43, v82, v30
	v_fmac_f32_e32 v40, v81, v30
	v_fmac_f32_e32 v41, v80, v30
	v_fmac_f32_e32 v38, v79, v30
	v_fmac_f32_e32 v39, v78, v30
	v_fmac_f32_e32 v36, v77, v30
	v_fmac_f32_e32 v37, v76, v30
	v_fmac_f32_e32 v34, v75, v30
	v_fmac_f32_e32 v35, v74, v30
	v_fmac_f32_e32 v32, v73, v30
	v_fmac_f32_e32 v33, v72, v30
	v_fma_f32 v30, v51, v30, v103
	v_fmac_f32_e32 v118, v102, v31
	v_fmac_f32_e32 v119, v101, v31
	v_fmac_f32_e32 v120, v99, v31
	v_fmac_f32_e32 v70, v98, v31
	v_fmac_f32_e32 v71, v97, v31
	v_fmac_f32_e32 v68, v96, v31
	v_fmac_f32_e32 v69, v95, v31
	v_fmac_f32_e32 v66, v94, v31
	v_fmac_f32_e32 v67, v93, v31
	v_fmac_f32_e32 v64, v92, v31
	v_fmac_f32_e32 v65, v91, v31
	v_fmac_f32_e32 v62, v90, v31
	v_fmac_f32_e32 v63, v89, v31
	v_fmac_f32_e32 v46, v88, v31
	v_fmac_f32_e32 v47, v87, v31
	v_fmac_f32_e32 v44, v86, v31
	v_fmac_f32_e32 v45, v85, v31
	v_fmac_f32_e32 v42, v84, v31
	v_fmac_f32_e32 v43, v83, v31
	v_fmac_f32_e32 v40, v82, v31
	v_fmac_f32_e32 v41, v81, v31
	v_fmac_f32_e32 v38, v80, v31
	v_fmac_f32_e32 v39, v79, v31
	v_fmac_f32_e32 v36, v78, v31
	v_fmac_f32_e32 v37, v77, v31
	v_fmac_f32_e32 v34, v76, v31
	v_fmac_f32_e32 v35, v75, v31
	v_fmac_f32_e32 v32, v74, v31
	v_fmac_f32_e32 v33, v73, v31
	v_fmac_f32_e32 v30, v72, v31
	v_fma_f32 v31, v51, v31, v103
	v_fmac_f32_e32 v30, v73, v28
	v_fmac_f32_e32 v31, v72, v28
	v_fmac_f32_e32 v30, v74, v29
	v_fmac_f32_e32 v31, v73, v29
	v_fmac_f32_e32 v33, v74, v28
	s_waitcnt lgkmcnt(13)
	v_fmac_f32_e32 v30, v75, v26
	v_fmac_f32_e32 v31, v74, v26
	v_fmac_f32_e32 v32, v75, v28
	v_fmac_f32_e32 v33, v75, v29
	v_fmac_f32_e32 v30, v76, v27
	v_fmac_f32_e32 v31, v75, v27
	v_fmac_f32_e32 v35, v76, v28
	v_fmac_f32_e32 v32, v76, v29
	v_fmac_f32_e32 v33, v76, v26
	s_waitcnt lgkmcnt(12)
	v_fmac_f32_e32 v30, v77, v24
	v_fmac_f32_e32 v31, v76, v24
	v_fmac_f32_e32 v34, v77, v28
	v_fmac_f32_e32 v35, v77, v29
	v_fmac_f32_e32 v32, v77, v26
	v_fmac_f32_e32 v33, v77, v27
	v_fmac_f32_e32 v30, v78, v25
	v_fmac_f32_e32 v31, v77, v25
	v_fmac_f32_e32 v37, v78, v28
	v_fmac_f32_e32 v34, v78, v29
	v_fmac_f32_e32 v35, v78, v26
	v_fmac_f32_e32 v32, v78, v27
	v_fmac_f32_e32 v33, v78, v24
	s_waitcnt lgkmcnt(11)
	v_fmac_f32_e32 v30, v79, v22
	v_fmac_f32_e32 v31, v78, v22
	v_fmac_f32_e32 v36, v79, v28
	v_fmac_f32_e32 v37, v79, v29
	v_fmac_f32_e32 v34, v79, v26
	v_fmac_f32_e32 v35, v79, v27
	v_fmac_f32_e32 v32, v79, v24
	v_fmac_f32_e32 v33, v79, v25
	v_fmac_f32_e32 v30, v80, v23
	v_fmac_f32_e32 v31, v79, v23
	v_fmac_f32_e32 v39, v80, v28
	v_fmac_f32_e32 v36, v80, v29
	v_fmac_f32_e32 v37, v80, v26
	v_fmac_f32_e32 v34, v80, v27
	v_fmac_f32_e32 v35, v80, v24
	v_fmac_f32_e32 v32, v80, v25
	v_fmac_f32_e32 v33, v80, v22
	s_waitcnt lgkmcnt(10)
	v_fmac_f32_e32 v30, v81, v20
	v_fmac_f32_e32 v31, v80, v20
	v_fmac_f32_e32 v38, v81, v28
	v_fmac_f32_e32 v39, v81, v29
	v_fmac_f32_e32 v36, v81, v26
	v_fmac_f32_e32 v37, v81, v27
	v_fmac_f32_e32 v34, v81, v24
	v_fmac_f32_e32 v35, v81, v25
	v_fmac_f32_e32 v32, v81, v22
	v_fmac_f32_e32 v33, v81, v23
	v_fmac_f32_e32 v30, v82, v21
	v_fmac_f32_e32 v31, v81, v21
	v_fmac_f32_e32 v41, v82, v28
	v_fmac_f32_e32 v38, v82, v29
	v_fmac_f32_e32 v39, v82, v26
	v_fmac_f32_e32 v36, v82, v27
	v_fmac_f32_e32 v37, v82, v24
	v_fmac_f32_e32 v34, v82, v25
	v_fmac_f32_e32 v35, v82, v22
	v_fmac_f32_e32 v32, v82, v23
	v_fmac_f32_e32 v33, v82, v20
	s_waitcnt lgkmcnt(9)
	v_fmac_f32_e32 v30, v83, v18
	v_fmac_f32_e32 v31, v82, v18
	v_fmac_f32_e32 v40, v83, v28
	v_fmac_f32_e32 v41, v83, v29
	v_fmac_f32_e32 v38, v83, v26
	v_fmac_f32_e32 v39, v83, v27
	v_fmac_f32_e32 v36, v83, v24
	v_fmac_f32_e32 v37, v83, v25
	v_fmac_f32_e32 v34, v83, v22
	v_fmac_f32_e32 v35, v83, v23
	v_fmac_f32_e32 v32, v83, v20
	v_fmac_f32_e32 v33, v83, v21
	v_fmac_f32_e32 v30, v84, v19
	v_fmac_f32_e32 v31, v83, v19
	v_fmac_f32_e32 v43, v84, v28
	v_fmac_f32_e32 v40, v84, v29
	v_fmac_f32_e32 v41, v84, v26
	v_fmac_f32_e32 v38, v84, v27
	v_fmac_f32_e32 v39, v84, v24
	v_fmac_f32_e32 v36, v84, v25
	v_fmac_f32_e32 v37, v84, v22
	v_fmac_f32_e32 v34, v84, v23
	v_fmac_f32_e32 v35, v84, v20
	v_fmac_f32_e32 v32, v84, v21
	v_fmac_f32_e32 v33, v84, v18
	s_waitcnt lgkmcnt(8)
	v_fmac_f32_e32 v30, v85, v16
	v_fmac_f32_e32 v31, v84, v16
	v_fmac_f32_e32 v42, v85, v28
	v_fmac_f32_e32 v43, v85, v29
	v_fmac_f32_e32 v40, v85, v26
	v_fmac_f32_e32 v41, v85, v27
	v_fmac_f32_e32 v38, v85, v24
	v_fmac_f32_e32 v39, v85, v25
	v_fmac_f32_e32 v36, v85, v22
	v_fmac_f32_e32 v37, v85, v23
	v_fmac_f32_e32 v34, v85, v20
	v_fmac_f32_e32 v35, v85, v21
	v_fmac_f32_e32 v32, v85, v18
	v_fmac_f32_e32 v33, v85, v19
	v_fmac_f32_e32 v30, v86, v17
	v_fmac_f32_e32 v31, v85, v17
	v_fmac_f32_e32 v45, v86, v28
	v_fmac_f32_e32 v42, v86, v29
	v_fmac_f32_e32 v43, v86, v26
	v_fmac_f32_e32 v40, v86, v27
	v_fmac_f32_e32 v41, v86, v24
	v_fmac_f32_e32 v38, v86, v25
	v_fmac_f32_e32 v39, v86, v22
	v_fmac_f32_e32 v36, v86, v23
	v_fmac_f32_e32 v37, v86, v20
	v_fmac_f32_e32 v34, v86, v21
	v_fmac_f32_e32 v35, v86, v18
	v_fmac_f32_e32 v32, v86, v19
	v_fmac_f32_e32 v33, v86, v16
	s_waitcnt lgkmcnt(7)
	v_fmac_f32_e32 v30, v87, v14
	v_fmac_f32_e32 v31, v86, v14
	v_fmac_f32_e32 v44, v87, v28
	v_fmac_f32_e32 v45, v87, v29
	v_fmac_f32_e32 v42, v87, v26
	v_fmac_f32_e32 v43, v87, v27
	v_fmac_f32_e32 v40, v87, v24
	v_fmac_f32_e32 v41, v87, v25
	v_fmac_f32_e32 v38, v87, v22
	v_fmac_f32_e32 v39, v87, v23
	v_fmac_f32_e32 v36, v87, v20
	v_fmac_f32_e32 v37, v87, v21
	v_fmac_f32_e32 v34, v87, v18
	v_fmac_f32_e32 v35, v87, v19
	v_fmac_f32_e32 v32, v87, v16
	v_fmac_f32_e32 v33, v87, v17
	v_fmac_f32_e32 v30, v88, v15
	v_fmac_f32_e32 v31, v87, v15
	v_fmac_f32_e32 v47, v88, v28
	v_fmac_f32_e32 v44, v88, v29
	v_fmac_f32_e32 v45, v88, v26
	v_fmac_f32_e32 v42, v88, v27
	v_fmac_f32_e32 v43, v88, v24
	v_fmac_f32_e32 v40, v88, v25
	v_fmac_f32_e32 v41, v88, v22
	v_fmac_f32_e32 v38, v88, v23
	v_fmac_f32_e32 v39, v88, v20
	v_fmac_f32_e32 v36, v88, v21
	v_fmac_f32_e32 v37, v88, v18
	v_fmac_f32_e32 v34, v88, v19
	v_fmac_f32_e32 v35, v88, v16
	v_fmac_f32_e32 v32, v88, v17
	v_fmac_f32_e32 v33, v88, v14
	s_waitcnt lgkmcnt(6)
	v_fmac_f32_e32 v30, v89, v12
	v_fmac_f32_e32 v31, v88, v12
	v_fmac_f32_e32 v46, v89, v28
	v_fmac_f32_e32 v47, v89, v29
	v_fmac_f32_e32 v44, v89, v26
	v_fmac_f32_e32 v45, v89, v27
	v_fmac_f32_e32 v42, v89, v24
	v_fmac_f32_e32 v43, v89, v25
	v_fmac_f32_e32 v40, v89, v22
	v_fmac_f32_e32 v41, v89, v23
	v_fmac_f32_e32 v38, v89, v20
	v_fmac_f32_e32 v39, v89, v21
	v_fmac_f32_e32 v36, v89, v18
	v_fmac_f32_e32 v37, v89, v19
	v_fmac_f32_e32 v34, v89, v16
	v_fmac_f32_e32 v35, v89, v17
	v_fmac_f32_e32 v32, v89, v14
	v_fmac_f32_e32 v33, v89, v15
	v_fmac_f32_e32 v30, v90, v13
	v_fmac_f32_e32 v31, v89, v13
	v_fmac_f32_e32 v63, v90, v28
	v_fmac_f32_e32 v46, v90, v29
	v_fmac_f32_e32 v47, v90, v26
	v_fmac_f32_e32 v44, v90, v27
	v_fmac_f32_e32 v45, v90, v24
	v_fmac_f32_e32 v42, v90, v25
	v_fmac_f32_e32 v43, v90, v22
	v_fmac_f32_e32 v40, v90, v23
	v_fmac_f32_e32 v41, v90, v20
	v_fmac_f32_e32 v38, v90, v21
	v_fmac_f32_e32 v39, v90, v18
	v_fmac_f32_e32 v36, v90, v19
	v_fmac_f32_e32 v37, v90, v16
	v_fmac_f32_e32 v34, v90, v17
	v_fmac_f32_e32 v35, v90, v14
	v_fmac_f32_e32 v32, v90, v15
	v_fmac_f32_e32 v33, v90, v12
	s_waitcnt lgkmcnt(5)
	v_fmac_f32_e32 v30, v91, v10
	v_fmac_f32_e32 v31, v90, v10
	v_fmac_f32_e32 v62, v91, v28
	v_fmac_f32_e32 v63, v91, v29
	v_fmac_f32_e32 v46, v91, v26
	v_fmac_f32_e32 v47, v91, v27
	v_fmac_f32_e32 v44, v91, v24
	v_fmac_f32_e32 v45, v91, v25
	v_fmac_f32_e32 v42, v91, v22
	v_fmac_f32_e32 v43, v91, v23
	v_fmac_f32_e32 v40, v91, v20
	v_fmac_f32_e32 v41, v91, v21
	v_fmac_f32_e32 v38, v91, v18
	v_fmac_f32_e32 v39, v91, v19
	v_fmac_f32_e32 v36, v91, v16
	v_fmac_f32_e32 v37, v91, v17
	v_fmac_f32_e32 v34, v91, v14
	v_fmac_f32_e32 v35, v91, v15
	v_fmac_f32_e32 v32, v91, v12
	v_fmac_f32_e32 v33, v91, v13
	v_fmac_f32_e32 v30, v92, v11
	v_fmac_f32_e32 v31, v91, v11
	v_fmac_f32_e32 v65, v92, v28
	v_fmac_f32_e32 v62, v92, v29
	v_fmac_f32_e32 v63, v92, v26
	v_fmac_f32_e32 v46, v92, v27
	v_fmac_f32_e32 v47, v92, v24
	v_fmac_f32_e32 v44, v92, v25
	v_fmac_f32_e32 v45, v92, v22
	v_fmac_f32_e32 v42, v92, v23
	v_fmac_f32_e32 v43, v92, v20
	v_fmac_f32_e32 v40, v92, v21
	v_fmac_f32_e32 v41, v92, v18
	v_fmac_f32_e32 v38, v92, v19
	v_fmac_f32_e32 v39, v92, v16
	v_fmac_f32_e32 v36, v92, v17
	v_fmac_f32_e32 v37, v92, v14
	v_fmac_f32_e32 v34, v92, v15
	v_fmac_f32_e32 v35, v92, v12
	v_fmac_f32_e32 v32, v92, v13
	v_fmac_f32_e32 v33, v92, v10
	s_waitcnt lgkmcnt(4)
	v_fmac_f32_e32 v30, v93, v8
	v_fmac_f32_e32 v31, v92, v8
	v_fmac_f32_e32 v64, v93, v28
	v_fmac_f32_e32 v65, v93, v29
	v_fmac_f32_e32 v62, v93, v26
	v_fmac_f32_e32 v63, v93, v27
	v_fmac_f32_e32 v46, v93, v24
	v_fmac_f32_e32 v47, v93, v25
	v_fmac_f32_e32 v44, v93, v22
	v_fmac_f32_e32 v45, v93, v23
	v_fmac_f32_e32 v42, v93, v20
	v_fmac_f32_e32 v43, v93, v21
	v_fmac_f32_e32 v40, v93, v18
	v_fmac_f32_e32 v41, v93, v19
	v_fmac_f32_e32 v38, v93, v16
	v_fmac_f32_e32 v39, v93, v17
	v_fmac_f32_e32 v36, v93, v14
	v_fmac_f32_e32 v37, v93, v15
	v_fmac_f32_e32 v34, v93, v12
	v_fmac_f32_e32 v35, v93, v13
	v_fmac_f32_e32 v32, v93, v10
	v_fmac_f32_e32 v33, v93, v11
	v_fmac_f32_e32 v30, v94, v9
	v_fmac_f32_e32 v31, v93, v9
	v_fmac_f32_e32 v67, v94, v28
	v_fmac_f32_e32 v64, v94, v29
	v_fmac_f32_e32 v65, v94, v26
	v_fmac_f32_e32 v62, v94, v27
	v_fmac_f32_e32 v63, v94, v24
	v_fmac_f32_e32 v46, v94, v25
	v_fmac_f32_e32 v47, v94, v22
	v_fmac_f32_e32 v44, v94, v23
	v_fmac_f32_e32 v45, v94, v20
	v_fmac_f32_e32 v42, v94, v21
	v_fmac_f32_e32 v43, v94, v18
	v_fmac_f32_e32 v40, v94, v19
	v_fmac_f32_e32 v41, v94, v16
	v_fmac_f32_e32 v38, v94, v17
	v_fmac_f32_e32 v39, v94, v14
	v_fmac_f32_e32 v36, v94, v15
	v_fmac_f32_e32 v37, v94, v12
	v_fmac_f32_e32 v34, v94, v13
	v_fmac_f32_e32 v35, v94, v10
	v_fmac_f32_e32 v32, v94, v11
	v_fmac_f32_e32 v33, v94, v8
	s_waitcnt lgkmcnt(3)
	v_fmac_f32_e32 v30, v95, v6
	v_fmac_f32_e32 v31, v94, v6
	v_fmac_f32_e32 v66, v95, v28
	v_fmac_f32_e32 v67, v95, v29
	v_fmac_f32_e32 v64, v95, v26
	v_fmac_f32_e32 v65, v95, v27
	v_fmac_f32_e32 v62, v95, v24
	v_fmac_f32_e32 v63, v95, v25
	v_fmac_f32_e32 v46, v95, v22
	v_fmac_f32_e32 v47, v95, v23
	v_fmac_f32_e32 v44, v95, v20
	v_fmac_f32_e32 v45, v95, v21
	v_fmac_f32_e32 v42, v95, v18
	v_fmac_f32_e32 v43, v95, v19
	v_fmac_f32_e32 v40, v95, v16
	v_fmac_f32_e32 v41, v95, v17
	v_fmac_f32_e32 v38, v95, v14
	v_fmac_f32_e32 v39, v95, v15
	v_fmac_f32_e32 v36, v95, v12
	v_fmac_f32_e32 v37, v95, v13
	v_fmac_f32_e32 v34, v95, v10
	v_fmac_f32_e32 v35, v95, v11
	v_fmac_f32_e32 v32, v95, v8
	v_fmac_f32_e32 v33, v95, v9
	v_fmac_f32_e32 v30, v96, v7
	v_fmac_f32_e32 v31, v95, v7
	v_fmac_f32_e32 v69, v96, v28
	v_fmac_f32_e32 v66, v96, v29
	v_fmac_f32_e32 v67, v96, v26
	v_fmac_f32_e32 v64, v96, v27
	v_fmac_f32_e32 v65, v96, v24
	v_fmac_f32_e32 v62, v96, v25
	v_fmac_f32_e32 v63, v96, v22
	v_fmac_f32_e32 v46, v96, v23
	v_fmac_f32_e32 v47, v96, v20
	v_fmac_f32_e32 v44, v96, v21
	v_fmac_f32_e32 v45, v96, v18
	v_fmac_f32_e32 v42, v96, v19
	v_fmac_f32_e32 v43, v96, v16
	v_fmac_f32_e32 v40, v96, v17
	v_fmac_f32_e32 v41, v96, v14
	v_fmac_f32_e32 v38, v96, v15
	v_fmac_f32_e32 v39, v96, v12
	v_fmac_f32_e32 v36, v96, v13
	v_fmac_f32_e32 v37, v96, v10
	v_fmac_f32_e32 v34, v96, v11
	v_fmac_f32_e32 v35, v96, v8
	v_fmac_f32_e32 v32, v96, v9
	v_fmac_f32_e32 v33, v96, v6
	s_waitcnt lgkmcnt(2)
	v_fmac_f32_e32 v30, v97, v4
	v_fmac_f32_e32 v31, v96, v4
	v_fmac_f32_e32 v68, v97, v28
	v_fmac_f32_e32 v69, v97, v29
	v_fmac_f32_e32 v66, v97, v26
	v_fmac_f32_e32 v67, v97, v27
	v_fmac_f32_e32 v64, v97, v24
	v_fmac_f32_e32 v65, v97, v25
	v_fmac_f32_e32 v62, v97, v22
	v_fmac_f32_e32 v63, v97, v23
	v_fmac_f32_e32 v46, v97, v20
	v_fmac_f32_e32 v47, v97, v21
	v_fmac_f32_e32 v44, v97, v18
	v_fmac_f32_e32 v45, v97, v19
	v_fmac_f32_e32 v42, v97, v16
	v_fmac_f32_e32 v43, v97, v17
	v_fmac_f32_e32 v40, v97, v14
	v_fmac_f32_e32 v41, v97, v15
	v_fmac_f32_e32 v38, v97, v12
	v_fmac_f32_e32 v39, v97, v13
	v_fmac_f32_e32 v36, v97, v10
	v_fmac_f32_e32 v37, v97, v11
	v_fmac_f32_e32 v34, v97, v8
	v_fmac_f32_e32 v35, v97, v9
	v_fmac_f32_e32 v32, v97, v6
	v_fmac_f32_e32 v33, v97, v7
	v_fmac_f32_e32 v30, v98, v5
	v_fmac_f32_e32 v31, v97, v5
	v_fmac_f32_e32 v71, v98, v28
	v_fmac_f32_e32 v68, v98, v29
	v_fmac_f32_e32 v69, v98, v26
	v_fmac_f32_e32 v66, v98, v27
	v_fmac_f32_e32 v67, v98, v24
	v_fmac_f32_e32 v64, v98, v25
	v_fmac_f32_e32 v65, v98, v22
	v_fmac_f32_e32 v62, v98, v23
	v_fmac_f32_e32 v63, v98, v20
	v_fmac_f32_e32 v46, v98, v21
	v_fmac_f32_e32 v47, v98, v18
	v_fmac_f32_e32 v44, v98, v19
	v_fmac_f32_e32 v45, v98, v16
	v_fmac_f32_e32 v42, v98, v17
	v_fmac_f32_e32 v43, v98, v14
	v_fmac_f32_e32 v40, v98, v15
	v_fmac_f32_e32 v41, v98, v12
	v_fmac_f32_e32 v38, v98, v13
	v_fmac_f32_e32 v39, v98, v10
	v_fmac_f32_e32 v36, v98, v11
	v_fmac_f32_e32 v37, v98, v8
	v_fmac_f32_e32 v34, v98, v9
	v_fmac_f32_e32 v35, v98, v6
	v_fmac_f32_e32 v32, v98, v7
	v_fmac_f32_e32 v33, v98, v4
	s_waitcnt lgkmcnt(1)
	v_fmac_f32_e32 v30, v99, v2
	v_fmac_f32_e32 v31, v98, v2
	v_fmac_f32_e32 v70, v99, v28
	v_fmac_f32_e32 v71, v99, v29
	v_fmac_f32_e32 v68, v99, v26
	v_fmac_f32_e32 v69, v99, v27
	v_fmac_f32_e32 v66, v99, v24
	v_fmac_f32_e32 v67, v99, v25
	v_fmac_f32_e32 v64, v99, v22
	v_fmac_f32_e32 v65, v99, v23
	v_fmac_f32_e32 v62, v99, v20
	v_fmac_f32_e32 v63, v99, v21
	v_fmac_f32_e32 v46, v99, v18
	v_fmac_f32_e32 v47, v99, v19
	v_fmac_f32_e32 v44, v99, v16
	v_fmac_f32_e32 v45, v99, v17
	v_fmac_f32_e32 v42, v99, v14
	v_fmac_f32_e32 v43, v99, v15
	v_fmac_f32_e32 v40, v99, v12
	v_fmac_f32_e32 v41, v99, v13
	v_fmac_f32_e32 v38, v99, v10
	v_fmac_f32_e32 v39, v99, v11
	v_fmac_f32_e32 v36, v99, v8
	v_fmac_f32_e32 v37, v99, v9
	v_fmac_f32_e32 v34, v99, v6
	v_fmac_f32_e32 v35, v99, v7
	v_fmac_f32_e32 v32, v99, v4
	v_fmac_f32_e32 v33, v99, v5
	v_fmac_f32_e32 v30, v101, v3
	v_fmac_f32_e32 v31, v99, v3
	v_fmac_f32_e32 v120, v101, v28
	v_fmac_f32_e32 v70, v101, v29
	v_fmac_f32_e32 v71, v101, v26
	v_fmac_f32_e32 v68, v101, v27
	v_fmac_f32_e32 v69, v101, v24
	v_fmac_f32_e32 v66, v101, v25
	v_fmac_f32_e32 v67, v101, v22
	v_fmac_f32_e32 v64, v101, v23
	v_fmac_f32_e32 v65, v101, v20
	v_fmac_f32_e32 v62, v101, v21
	v_fmac_f32_e32 v63, v101, v18
	v_fmac_f32_e32 v46, v101, v19
	v_fmac_f32_e32 v47, v101, v16
	v_fmac_f32_e32 v44, v101, v17
	v_fmac_f32_e32 v45, v101, v14
	v_fmac_f32_e32 v42, v101, v15
	v_fmac_f32_e32 v43, v101, v12
	v_fmac_f32_e32 v40, v101, v13
	v_fmac_f32_e32 v41, v101, v10
	v_fmac_f32_e32 v38, v101, v11
	v_fmac_f32_e32 v39, v101, v8
	v_fmac_f32_e32 v36, v101, v9
	v_fmac_f32_e32 v37, v101, v6
	v_fmac_f32_e32 v34, v101, v7
	v_fmac_f32_e32 v35, v101, v4
	v_fmac_f32_e32 v32, v101, v5
	v_fmac_f32_e32 v33, v101, v2
	s_waitcnt lgkmcnt(0)
	v_fmac_f32_e32 v30, v102, v0
	v_fmac_f32_e32 v31, v101, v0
	v_add_u32_e32 v0, s6, v105
	v_fmac_f32_e32 v119, v102, v28
	v_fmac_f32_e32 v120, v102, v29
	v_fmac_f32_e32 v70, v102, v26
	v_fmac_f32_e32 v71, v102, v27
	v_fmac_f32_e32 v68, v102, v24
	v_fmac_f32_e32 v69, v102, v25
	v_fmac_f32_e32 v66, v102, v22
	v_fmac_f32_e32 v67, v102, v23
	v_fmac_f32_e32 v64, v102, v20
	v_fmac_f32_e32 v65, v102, v21
	v_fmac_f32_e32 v62, v102, v18
	v_fmac_f32_e32 v63, v102, v19
	v_fmac_f32_e32 v46, v102, v16
	v_fmac_f32_e32 v47, v102, v17
	v_fmac_f32_e32 v44, v102, v14
	v_fmac_f32_e32 v45, v102, v15
	v_fmac_f32_e32 v42, v102, v12
	v_fmac_f32_e32 v43, v102, v13
	v_fmac_f32_e32 v40, v102, v10
	v_fmac_f32_e32 v41, v102, v11
	v_fmac_f32_e32 v38, v102, v8
	v_fmac_f32_e32 v39, v102, v9
	v_fmac_f32_e32 v36, v102, v6
	v_fmac_f32_e32 v37, v102, v7
	v_fmac_f32_e32 v34, v102, v4
	v_fmac_f32_e32 v35, v102, v5
	v_fmac_f32_e32 v32, v102, v2
	v_fmac_f32_e32 v33, v102, v3
	v_fmac_f32_e32 v31, v102, v1
	s_barrier
	ds_write2st64_b32 v104, v117, v118 offset1:4
	ds_write2st64_b32 v104, v119, v120 offset0:8 offset1:12
	ds_write2st64_b32 v104, v70, v71 offset0:16 offset1:20
	ds_write2st64_b32 v104, v68, v69 offset0:24 offset1:28
	ds_write2st64_b32 v104, v66, v67 offset0:32 offset1:36
	ds_write2st64_b32 v104, v64, v65 offset0:40 offset1:44
	ds_write2st64_b32 v104, v62, v63 offset0:48 offset1:52
	ds_write2st64_b32 v104, v46, v47 offset0:56 offset1:60
	ds_write2st64_b32 v104, v44, v45 offset0:64 offset1:68
	ds_write2st64_b32 v104, v42, v43 offset0:72 offset1:76
	ds_write2st64_b32 v104, v40, v41 offset0:80 offset1:84
	ds_write2st64_b32 v104, v38, v39 offset0:88 offset1:92
	ds_write2st64_b32 v104, v36, v37 offset0:96 offset1:100
	ds_write2st64_b32 v104, v34, v35 offset0:104 offset1:108
	ds_write2st64_b32 v104, v32, v33 offset0:112 offset1:116
	ds_write2st64_b32 v104, v30, v31 offset0:120 offset1:124
	s_waitcnt lgkmcnt(0)
	s_barrier
	ds_read_b128 v[0:3], v0
	v_add_u32_e32 v12, s17, v105
	s_lshl_b64 s[0:1], s[2:3], 12
	s_ashr_i32 s2, s51, 31
	s_add_u32 s4, s0, s51
	s_waitcnt lgkmcnt(0)
	v_add_f32_e32 v4, v0, v1
	v_add_f32_e32 v4, v2, v4
	v_add_f32_e32 v4, v3, v4
	ds_swizzle_b32 v5, v4 offset:swizzle(SWAP,1)
	s_addc_u32 s5, s1, s2
	s_add_u32 s0, s4, s15
	s_addc_u32 s1, s5, s7
	s_lshl_b64 s[0:1], s[0:1], 11
	s_waitcnt lgkmcnt(0)
	v_add_f32_e32 v4, v4, v5
	ds_swizzle_b32 v5, v4 offset:swizzle(SWAP,2)
	s_mov_b32 s52, 0x3b800000
	s_waitcnt lgkmcnt(0)
	v_add_f32_e32 v4, v4, v5
	ds_swizzle_b32 v5, v4 offset:swizzle(SWAP,4)
	s_waitcnt lgkmcnt(0)
	v_add_f32_e32 v4, v4, v5
	ds_swizzle_b32 v5, v4 offset:swizzle(SWAP,8)
	s_waitcnt lgkmcnt(0)
	v_add_f32_e32 v4, v4, v5
	ds_swizzle_b32 v5, v4 offset:swizzle(SWAP,16)
	s_waitcnt lgkmcnt(0)
	v_add_f32_e32 v4, v4, v5
	v_mov_b32_e32 v5, v4
	s_nop 1
	v_permlane32_swap_b32_e32 v4, v5
	v_add_f32_e32 v4, v4, v5
	v_fmamk_f32 v19, v4, 0xbb800000, v1
	v_fmamk_f32 v18, v4, 0xbb800000, v0
	v_fmamk_f32 v3, v4, 0xbb800000, v3
	v_fmac_f32_e32 v2, 0xbb800000, v4
	v_pk_mul_f32 v[4:5], v[18:19], v[18:19]
	v_pk_mul_f32 v[0:1], v[2:3], v[2:3]
	v_add_f32_e32 v4, v4, v5
	v_add_f32_e32 v0, v0, v4
	global_load_dwordx4 v[172:175], v[56:57], off
	global_load_dwordx4 v[176:179], v[58:59], off
	ds_read_b128 v[12:15], v12
	v_add_f32_e32 v0, v1, v0
	ds_swizzle_b32 v1, v0 offset:swizzle(SWAP,1)
	s_waitcnt lgkmcnt(1)
	v_add_f32_e32 v16, v12, v13
	v_add_f32_e32 v16, v14, v16
	v_add_f32_e32 v16, v15, v16
	ds_swizzle_b32 v20, v16 offset:swizzle(SWAP,1)
	s_waitcnt lgkmcnt(1)
	v_add_f32_e32 v0, v0, v1
	ds_swizzle_b32 v1, v0 offset:swizzle(SWAP,2)
	s_waitcnt lgkmcnt(1)
	v_add_f32_e32 v16, v16, v20
	ds_swizzle_b32 v20, v16 offset:swizzle(SWAP,2)
	s_waitcnt lgkmcnt(1)
	v_add_f32_e32 v0, v0, v1
	ds_swizzle_b32 v1, v0 offset:swizzle(SWAP,4)
	s_waitcnt lgkmcnt(1)
	v_add_f32_e32 v16, v16, v20
	ds_swizzle_b32 v20, v16 offset:swizzle(SWAP,4)
	s_waitcnt lgkmcnt(1)
	v_add_f32_e32 v0, v0, v1
	ds_swizzle_b32 v1, v0 offset:swizzle(SWAP,8)
	s_waitcnt lgkmcnt(1)
	v_add_f32_e32 v16, v16, v20
	ds_swizzle_b32 v20, v16 offset:swizzle(SWAP,8)
	s_waitcnt lgkmcnt(1)
	v_add_f32_e32 v0, v0, v1
	ds_swizzle_b32 v1, v0 offset:swizzle(SWAP,16)
	s_waitcnt lgkmcnt(1)
	v_add_f32_e32 v16, v16, v20
	ds_swizzle_b32 v20, v16 offset:swizzle(SWAP,16)
	s_waitcnt lgkmcnt(1)
	v_add_f32_e32 v17, v0, v1
	v_mov_b32_e32 v21, v17
	s_nop 1
	v_permlane32_swap_b32_e32 v17, v21
	s_waitcnt lgkmcnt(0)
	v_add_f32_e32 v16, v16, v20
	v_mov_b32_e32 v20, v16
	s_nop 1
	v_permlane32_swap_b32_e32 v16, v20
	v_add_f32_e32 v16, v16, v20
	v_fmamk_f32 v13, v16, 0xbb800000, v13
	v_fmamk_f32 v12, v16, 0xbb800000, v12
	v_fmamk_f32 v15, v16, 0xbb800000, v15
	v_fmac_f32_e32 v14, 0xbb800000, v16
	v_pk_mul_f32 v[24:25], v[12:13], v[12:13]
	v_pk_mul_f32 v[22:23], v[14:15], v[14:15]
	v_add_f32_e32 v16, v24, v25
	v_add_f32_e32 v16, v22, v16
	v_add_f32_e32 v16, v23, v16
	ds_swizzle_b32 v20, v16 offset:swizzle(SWAP,1)
	v_lshl_add_u64 v[0:1], v[60:61], 0, s[0:1]
	s_mov_b32 s0, 0x3727c5ac
	s_waitcnt lgkmcnt(0)
	v_add_f32_e32 v16, v16, v20
	ds_swizzle_b32 v20, v16 offset:swizzle(SWAP,2)
	s_waitcnt lgkmcnt(0)
	v_add_f32_e32 v16, v16, v20
	ds_swizzle_b32 v20, v16 offset:swizzle(SWAP,4)
	s_waitcnt lgkmcnt(0)
	v_add_f32_e32 v16, v16, v20
	ds_swizzle_b32 v20, v16 offset:swizzle(SWAP,8)
	s_waitcnt lgkmcnt(0)
	v_add_f32_e32 v16, v16, v20
	ds_swizzle_b32 v20, v16 offset:swizzle(SWAP,16)
	s_waitcnt lgkmcnt(0)
	v_add_f32_e32 v16, v16, v20
	v_mov_b32_e32 v20, v16
	s_nop 1
	v_permlane32_swap_b32_e32 v16, v20
	v_pk_add_f32 v[20:21], v[16:17], v[20:21]
	v_mov_b64_e32 v[16:17], s[0:1]
	v_pk_fma_f32 v[20:21], v[20:21], s[52:53], v[16:17] op_sel_hi:[1,0,0]
	s_nop 0
	v_mul_f32_e32 v22, 0x4b800000, v21
	v_cmp_gt_f32_e64 s[2:3], s56, v21
	v_cmp_gt_f32_e64 s[0:1], s56, v20
	s_nop 0
	v_cndmask_b32_e64 v21, v21, v22, s[2:3]
	v_rsq_f32_e32 v21, v21
	s_nop 0
	v_mul_f32_e32 v22, 0x45800000, v21
	v_cndmask_b32_e64 v22, v21, v22, s[2:3]
	v_pk_mul_f32 v[18:19], v[18:19], v[22:23] op_sel_hi:[1,0]
	v_pk_mul_f32 v[2:3], v[2:3], v[22:23] op_sel_hi:[1,0]
	s_waitcnt vmcnt(0)
	v_mov_b64_e32 v[4:5], v[172:173]
	v_mov_b64_e32 v[6:7], v[174:175]
	v_mov_b64_e32 v[8:9], v[176:177]
	v_mov_b64_e32 v[10:11], v[178:179]
	v_pk_fma_f32 v[4:5], v[4:5], v[18:19], v[8:9]
	v_pk_fma_f32 v[2:3], v[6:7], v[2:3], v[10:11]
	v_mul_f32_e32 v6, 0xbfb8aa3b, v4
	v_mul_f32_e32 v7, 0xbfb8aa3b, v5
	v_exp_f32_e32 v6, v6
	v_exp_f32_e32 v7, v7
	v_add_f32_e32 v6, 1.0, v6
	v_add_f32_e32 v7, 1.0, v7
	v_rcp_f32_e32 v6, v6
	v_rcp_f32_e32 v7, v7
	s_nop 0
	v_pk_mul_f32 v[4:5], v[4:5], v[6:7]
	s_nop 0
	v_cvt_pk_bf16_f32 v4, v4, v5
	v_mul_f32_e32 v5, 0xbfb8aa3b, v2
	v_exp_f32_e32 v5, v5
	s_nop 0
	v_add_f32_e32 v5, 1.0, v5
	v_rcp_f32_e32 v6, v5
	v_mul_f32_e32 v5, 0xbfb8aa3b, v3
	v_exp_f32_e32 v5, v5
	s_nop 0
	v_add_f32_e32 v5, 1.0, v5
	v_rcp_f32_e32 v7, v5
	s_nop 0
	v_pk_mul_f32 v[2:3], v[2:3], v[6:7]
	s_nop 0
	v_cvt_pk_bf16_f32 v5, v2, v3
	global_store_dwordx2 v[0:1], v[4:5], off
	v_mul_f32_e32 v0, 0x4b800000, v20
	v_cndmask_b32_e64 v0, v20, v0, s[0:1]
	v_rsq_f32_e32 v0, v0
	s_nop 0
	v_mul_f32_e32 v1, 0x45800000, v0
	v_cndmask_b32_e64 v8, v0, v1, s[0:1]
	v_mov_b64_e32 v[0:1], v[172:173]
	v_mov_b64_e32 v[2:3], v[174:175]
	v_mov_b64_e32 v[4:5], v[176:177]
	v_mov_b64_e32 v[6:7], v[178:179]
	v_pk_mul_f32 v[10:11], v[12:13], v[8:9] op_sel_hi:[1,0]
	v_pk_mul_f32 v[8:9], v[14:15], v[8:9] op_sel_hi:[1,0]
	s_add_u32 s0, s4, s16
	s_addc_u32 s1, s5, s18
	s_lshl_b64 s[0:1], s[0:1], 11
	v_add_u32_e32 v12, s23, v105
	v_pk_fma_f32 v[0:1], v[0:1], v[10:11], v[4:5]
	s_nop 0
	v_mul_f32_e32 v4, 0xbfb8aa3b, v0
	v_mul_f32_e32 v5, 0xbfb8aa3b, v1
	v_exp_f32_e32 v4, v4
	v_exp_f32_e32 v5, v5
	v_pk_fma_f32 v[2:3], v[2:3], v[8:9], v[6:7]
	v_add_f32_e32 v4, 1.0, v4
	v_add_f32_e32 v5, 1.0, v5
	v_rcp_f32_e32 v4, v4
	v_rcp_f32_e32 v5, v5
	s_nop 0
	v_pk_mul_f32 v[0:1], v[0:1], v[4:5]
	s_nop 0
	v_cvt_pk_bf16_f32 v0, v0, v1
	v_mul_f32_e32 v1, 0xbfb8aa3b, v2
	v_exp_f32_e32 v1, v1
	s_nop 0
	v_add_f32_e32 v1, 1.0, v1
	v_rcp_f32_e32 v4, v1
	v_mul_f32_e32 v1, 0xbfb8aa3b, v3
	v_exp_f32_e32 v1, v1
	s_nop 0
	v_add_f32_e32 v1, 1.0, v1
	v_rcp_f32_e32 v5, v1
	s_nop 0
	v_pk_mul_f32 v[2:3], v[2:3], v[4:5]
	s_nop 0
	v_cvt_pk_bf16_f32 v1, v2, v3
	v_lshl_add_u64 v[2:3], v[60:61], 0, s[0:1]
	global_store_dwordx2 v[2:3], v[0:1], off
	v_add_u32_e32 v0, s20, v105
	ds_read_b128 v[0:3], v0
	s_add_u32 s0, s4, s19
	s_addc_u32 s1, s5, s21
	s_lshl_b64 s[0:1], s[0:1], 11
	s_waitcnt lgkmcnt(0)
	v_add_f32_e32 v4, v0, v1
	v_add_f32_e32 v4, v2, v4
	v_add_f32_e32 v4, v3, v4
	ds_swizzle_b32 v5, v4 offset:swizzle(SWAP,1)
	s_waitcnt lgkmcnt(0)
	v_add_f32_e32 v4, v4, v5
	ds_swizzle_b32 v5, v4 offset:swizzle(SWAP,2)
	s_waitcnt lgkmcnt(0)
	v_add_f32_e32 v4, v4, v5
	ds_swizzle_b32 v5, v4 offset:swizzle(SWAP,4)
	s_waitcnt lgkmcnt(0)
	v_add_f32_e32 v4, v4, v5
	ds_swizzle_b32 v5, v4 offset:swizzle(SWAP,8)
	s_waitcnt lgkmcnt(0)
	v_add_f32_e32 v4, v4, v5
	ds_swizzle_b32 v5, v4 offset:swizzle(SWAP,16)
	s_waitcnt lgkmcnt(0)
	v_add_f32_e32 v4, v4, v5
	v_mov_b32_e32 v5, v4
	s_nop 1
	v_permlane32_swap_b32_e32 v4, v5
	v_add_f32_e32 v4, v4, v5
	v_fmamk_f32 v19, v4, 0xbb800000, v1
	v_fmamk_f32 v18, v4, 0xbb800000, v0
	v_fmamk_f32 v3, v4, 0xbb800000, v3
	v_fmac_f32_e32 v2, 0xbb800000, v4
	v_pk_mul_f32 v[4:5], v[18:19], v[18:19]
	v_pk_mul_f32 v[0:1], v[2:3], v[2:3]
	v_add_f32_e32 v4, v4, v5
	v_add_f32_e32 v0, v0, v4
	v_mov_b64_e32 v[4:5], v[172:173]
	v_mov_b64_e32 v[6:7], v[174:175]
	v_mov_b64_e32 v[8:9], v[176:177]
	v_mov_b64_e32 v[10:11], v[178:179]
	ds_read_b128 v[12:15], v12
	v_add_f32_e32 v0, v1, v0
	ds_swizzle_b32 v1, v0 offset:swizzle(SWAP,1)
	s_waitcnt lgkmcnt(1)
	v_add_f32_e32 v20, v12, v13
	v_add_f32_e32 v20, v14, v20
	v_add_f32_e32 v20, v15, v20
	ds_swizzle_b32 v22, v20 offset:swizzle(SWAP,1)
	s_waitcnt lgkmcnt(1)
	v_add_f32_e32 v0, v0, v1
	ds_swizzle_b32 v1, v0 offset:swizzle(SWAP,2)
	s_waitcnt lgkmcnt(1)
	v_add_f32_e32 v20, v20, v22
	ds_swizzle_b32 v22, v20 offset:swizzle(SWAP,2)
	s_waitcnt lgkmcnt(1)
	v_add_f32_e32 v0, v0, v1
	ds_swizzle_b32 v1, v0 offset:swizzle(SWAP,4)
	s_waitcnt lgkmcnt(1)
	v_add_f32_e32 v20, v20, v22
	ds_swizzle_b32 v22, v20 offset:swizzle(SWAP,4)
	s_waitcnt lgkmcnt(1)
	v_add_f32_e32 v0, v0, v1
	ds_swizzle_b32 v1, v0 offset:swizzle(SWAP,8)
	s_waitcnt lgkmcnt(1)
	v_add_f32_e32 v20, v20, v22
	ds_swizzle_b32 v22, v20 offset:swizzle(SWAP,8)
	s_waitcnt lgkmcnt(1)
	v_add_f32_e32 v0, v0, v1
	ds_swizzle_b32 v1, v0 offset:swizzle(SWAP,16)
	s_waitcnt lgkmcnt(1)
	v_add_f32_e32 v20, v20, v22
	ds_swizzle_b32 v22, v20 offset:swizzle(SWAP,16)
	s_waitcnt lgkmcnt(1)
	v_add_f32_e32 v21, v0, v1
	v_mov_b32_e32 v23, v21
	s_nop 1
	v_permlane32_swap_b32_e32 v21, v23
	s_waitcnt lgkmcnt(0)
	v_add_f32_e32 v20, v20, v22
	v_mov_b32_e32 v22, v20
	s_nop 1
	v_permlane32_swap_b32_e32 v20, v22
	v_add_f32_e32 v20, v20, v22
	v_fmamk_f32 v13, v20, 0xbb800000, v13
	v_fmamk_f32 v12, v20, 0xbb800000, v12
	v_fmamk_f32 v15, v20, 0xbb800000, v15
	v_fmac_f32_e32 v14, 0xbb800000, v20
	v_pk_mul_f32 v[26:27], v[12:13], v[12:13]
	v_pk_mul_f32 v[24:25], v[14:15], v[14:15]
	v_add_f32_e32 v20, v26, v27
	v_add_f32_e32 v20, v24, v20
	v_add_f32_e32 v20, v25, v20
	ds_swizzle_b32 v22, v20 offset:swizzle(SWAP,1)
	v_lshl_add_u64 v[0:1], v[60:61], 0, s[0:1]
	s_waitcnt lgkmcnt(0)
	v_add_f32_e32 v20, v20, v22
	ds_swizzle_b32 v22, v20 offset:swizzle(SWAP,2)
	s_waitcnt lgkmcnt(0)
	v_add_f32_e32 v20, v20, v22
	ds_swizzle_b32 v22, v20 offset:swizzle(SWAP,4)
	s_waitcnt lgkmcnt(0)
	v_add_f32_e32 v20, v20, v22
	ds_swizzle_b32 v22, v20 offset:swizzle(SWAP,8)
	s_waitcnt lgkmcnt(0)
	v_add_f32_e32 v20, v20, v22
	ds_swizzle_b32 v22, v20 offset:swizzle(SWAP,16)
	s_waitcnt lgkmcnt(0)
	v_add_f32_e32 v20, v20, v22
	v_mov_b32_e32 v22, v20
	s_nop 1
	v_permlane32_swap_b32_e32 v20, v22
	v_pk_add_f32 v[20:21], v[20:21], v[22:23]
	s_nop 0
	v_pk_fma_f32 v[20:21], v[20:21], s[52:53], v[16:17] op_sel_hi:[1,0,0]
	s_nop 0
	v_mul_f32_e32 v22, 0x4b800000, v21
	v_cmp_gt_f32_e64 s[2:3], s56, v21
	v_cmp_gt_f32_e64 s[0:1], s56, v20
	s_nop 0
	v_cndmask_b32_e64 v21, v21, v22, s[2:3]
	v_rsq_f32_e32 v21, v21
	s_nop 0
	v_mul_f32_e32 v22, 0x45800000, v21
	v_cndmask_b32_e64 v22, v21, v22, s[2:3]
	v_pk_mul_f32 v[18:19], v[18:19], v[22:23] op_sel_hi:[1,0]
	v_pk_mul_f32 v[2:3], v[2:3], v[22:23] op_sel_hi:[1,0]
	v_pk_fma_f32 v[4:5], v[4:5], v[18:19], v[8:9]
	v_pk_fma_f32 v[2:3], v[6:7], v[2:3], v[10:11]
	v_mul_f32_e32 v6, 0xbfb8aa3b, v4
	v_mul_f32_e32 v7, 0xbfb8aa3b, v5
	v_exp_f32_e32 v6, v6
	v_exp_f32_e32 v7, v7
	v_add_f32_e32 v6, 1.0, v6
	v_add_f32_e32 v7, 1.0, v7
	v_rcp_f32_e32 v6, v6
	v_rcp_f32_e32 v7, v7
	s_nop 0
	v_pk_mul_f32 v[4:5], v[4:5], v[6:7]
	s_nop 0
	v_cvt_pk_bf16_f32 v4, v4, v5
	v_mul_f32_e32 v5, 0xbfb8aa3b, v2
	v_exp_f32_e32 v5, v5
	s_nop 0
	v_add_f32_e32 v5, 1.0, v5
	v_rcp_f32_e32 v6, v5
	v_mul_f32_e32 v5, 0xbfb8aa3b, v3
	v_exp_f32_e32 v5, v5
	s_nop 0
	v_add_f32_e32 v5, 1.0, v5
	v_rcp_f32_e32 v7, v5
	s_nop 0
	v_pk_mul_f32 v[2:3], v[2:3], v[6:7]
	s_nop 0
	v_cvt_pk_bf16_f32 v5, v2, v3
	global_store_dwordx2 v[0:1], v[4:5], off
	v_mul_f32_e32 v0, 0x4b800000, v20
	v_cndmask_b32_e64 v0, v20, v0, s[0:1]
	v_rsq_f32_e32 v0, v0
	s_nop 0
	v_mul_f32_e32 v1, 0x45800000, v0
	v_cndmask_b32_e64 v8, v0, v1, s[0:1]
	v_mov_b64_e32 v[0:1], v[172:173]
	v_mov_b64_e32 v[2:3], v[174:175]
	v_mov_b64_e32 v[4:5], v[176:177]
	v_mov_b64_e32 v[6:7], v[178:179]
	v_pk_mul_f32 v[10:11], v[12:13], v[8:9] op_sel_hi:[1,0]
	v_pk_mul_f32 v[8:9], v[14:15], v[8:9] op_sel_hi:[1,0]
	s_add_u32 s0, s4, s22
	s_addc_u32 s1, s5, s24
	s_lshl_b64 s[0:1], s[0:1], 11
	v_add_u32_e32 v12, s29, v105
	v_pk_fma_f32 v[0:1], v[0:1], v[10:11], v[4:5]
	s_nop 0
	v_mul_f32_e32 v4, 0xbfb8aa3b, v0
	v_mul_f32_e32 v5, 0xbfb8aa3b, v1
	v_exp_f32_e32 v4, v4
	v_exp_f32_e32 v5, v5
	v_pk_fma_f32 v[2:3], v[2:3], v[8:9], v[6:7]
	v_add_f32_e32 v4, 1.0, v4
	v_add_f32_e32 v5, 1.0, v5
	v_rcp_f32_e32 v4, v4
	v_rcp_f32_e32 v5, v5
	s_nop 0
	v_pk_mul_f32 v[0:1], v[0:1], v[4:5]
	s_nop 0
	v_cvt_pk_bf16_f32 v0, v0, v1
	v_mul_f32_e32 v1, 0xbfb8aa3b, v2
	v_exp_f32_e32 v1, v1
	s_nop 0
	v_add_f32_e32 v1, 1.0, v1
	v_rcp_f32_e32 v4, v1
	v_mul_f32_e32 v1, 0xbfb8aa3b, v3
	v_exp_f32_e32 v1, v1
	s_nop 0
	v_add_f32_e32 v1, 1.0, v1
	v_rcp_f32_e32 v5, v1
	s_nop 0
	v_pk_mul_f32 v[2:3], v[2:3], v[4:5]
	s_nop 0
	v_cvt_pk_bf16_f32 v1, v2, v3
	v_lshl_add_u64 v[2:3], v[60:61], 0, s[0:1]
	global_store_dwordx2 v[2:3], v[0:1], off
	v_add_u32_e32 v0, s26, v105
	ds_read_b128 v[0:3], v0
	s_add_u32 s0, s4, s25
	s_addc_u32 s1, s5, s27
	s_lshl_b64 s[0:1], s[0:1], 11
	s_waitcnt lgkmcnt(0)
	v_add_f32_e32 v4, v0, v1
	v_add_f32_e32 v4, v2, v4
	v_add_f32_e32 v4, v3, v4
	ds_swizzle_b32 v5, v4 offset:swizzle(SWAP,1)
	s_waitcnt lgkmcnt(0)
	v_add_f32_e32 v4, v4, v5
	ds_swizzle_b32 v5, v4 offset:swizzle(SWAP,2)
	s_waitcnt lgkmcnt(0)
	v_add_f32_e32 v4, v4, v5
	ds_swizzle_b32 v5, v4 offset:swizzle(SWAP,4)
	s_waitcnt lgkmcnt(0)
	v_add_f32_e32 v4, v4, v5
	ds_swizzle_b32 v5, v4 offset:swizzle(SWAP,8)
	s_waitcnt lgkmcnt(0)
	v_add_f32_e32 v4, v4, v5
	ds_swizzle_b32 v5, v4 offset:swizzle(SWAP,16)
	s_waitcnt lgkmcnt(0)
	v_add_f32_e32 v4, v4, v5
	v_mov_b32_e32 v5, v4
	s_nop 1
	v_permlane32_swap_b32_e32 v4, v5
	v_add_f32_e32 v4, v4, v5
	v_fmamk_f32 v19, v4, 0xbb800000, v1
	v_fmamk_f32 v18, v4, 0xbb800000, v0
	v_fmamk_f32 v3, v4, 0xbb800000, v3
	v_fmac_f32_e32 v2, 0xbb800000, v4
	v_pk_mul_f32 v[4:5], v[18:19], v[18:19]
	v_pk_mul_f32 v[0:1], v[2:3], v[2:3]
	v_add_f32_e32 v4, v4, v5
	v_add_f32_e32 v0, v0, v4
	v_mov_b64_e32 v[4:5], v[172:173]
	v_mov_b64_e32 v[6:7], v[174:175]
	v_mov_b64_e32 v[8:9], v[176:177]
	v_mov_b64_e32 v[10:11], v[178:179]
	ds_read_b128 v[12:15], v12
	v_add_f32_e32 v0, v1, v0
	ds_swizzle_b32 v1, v0 offset:swizzle(SWAP,1)
	s_waitcnt lgkmcnt(1)
	v_add_f32_e32 v20, v12, v13
	v_add_f32_e32 v20, v14, v20
	v_add_f32_e32 v20, v15, v20
	ds_swizzle_b32 v22, v20 offset:swizzle(SWAP,1)
	s_waitcnt lgkmcnt(1)
	v_add_f32_e32 v0, v0, v1
	ds_swizzle_b32 v1, v0 offset:swizzle(SWAP,2)
	s_waitcnt lgkmcnt(1)
	v_add_f32_e32 v20, v20, v22
	ds_swizzle_b32 v22, v20 offset:swizzle(SWAP,2)
	s_waitcnt lgkmcnt(1)
	v_add_f32_e32 v0, v0, v1
	ds_swizzle_b32 v1, v0 offset:swizzle(SWAP,4)
	s_waitcnt lgkmcnt(1)
	v_add_f32_e32 v20, v20, v22
	ds_swizzle_b32 v22, v20 offset:swizzle(SWAP,4)
	s_waitcnt lgkmcnt(1)
	v_add_f32_e32 v0, v0, v1
	ds_swizzle_b32 v1, v0 offset:swizzle(SWAP,8)
	s_waitcnt lgkmcnt(1)
	v_add_f32_e32 v20, v20, v22
	ds_swizzle_b32 v22, v20 offset:swizzle(SWAP,8)
	s_waitcnt lgkmcnt(1)
	v_add_f32_e32 v0, v0, v1
	ds_swizzle_b32 v1, v0 offset:swizzle(SWAP,16)
	s_waitcnt lgkmcnt(1)
	v_add_f32_e32 v20, v20, v22
	ds_swizzle_b32 v22, v20 offset:swizzle(SWAP,16)
	s_waitcnt lgkmcnt(1)
	v_add_f32_e32 v21, v0, v1
	v_mov_b32_e32 v23, v21
	s_nop 1
	v_permlane32_swap_b32_e32 v21, v23
	s_waitcnt lgkmcnt(0)
	v_add_f32_e32 v20, v20, v22
	v_mov_b32_e32 v22, v20
	s_nop 1
	v_permlane32_swap_b32_e32 v20, v22
	v_add_f32_e32 v20, v20, v22
	v_fmamk_f32 v13, v20, 0xbb800000, v13
	v_fmamk_f32 v12, v20, 0xbb800000, v12
	v_fmamk_f32 v15, v20, 0xbb800000, v15
	v_fmac_f32_e32 v14, 0xbb800000, v20
	v_pk_mul_f32 v[26:27], v[12:13], v[12:13]
	v_pk_mul_f32 v[24:25], v[14:15], v[14:15]
	v_add_f32_e32 v20, v26, v27
	v_add_f32_e32 v20, v24, v20
	v_add_f32_e32 v20, v25, v20
	ds_swizzle_b32 v22, v20 offset:swizzle(SWAP,1)
	v_lshl_add_u64 v[0:1], v[60:61], 0, s[0:1]
	s_waitcnt lgkmcnt(0)
	v_add_f32_e32 v20, v20, v22
	ds_swizzle_b32 v22, v20 offset:swizzle(SWAP,2)
	s_waitcnt lgkmcnt(0)
	v_add_f32_e32 v20, v20, v22
	ds_swizzle_b32 v22, v20 offset:swizzle(SWAP,4)
	s_waitcnt lgkmcnt(0)
	v_add_f32_e32 v20, v20, v22
	ds_swizzle_b32 v22, v20 offset:swizzle(SWAP,8)
	s_waitcnt lgkmcnt(0)
	v_add_f32_e32 v20, v20, v22
	ds_swizzle_b32 v22, v20 offset:swizzle(SWAP,16)
	s_waitcnt lgkmcnt(0)
	v_add_f32_e32 v20, v20, v22
	v_mov_b32_e32 v22, v20
	s_nop 1
	v_permlane32_swap_b32_e32 v20, v22
	v_pk_add_f32 v[20:21], v[20:21], v[22:23]
	s_nop 0
	v_pk_fma_f32 v[20:21], v[20:21], s[52:53], v[16:17] op_sel_hi:[1,0,0]
	s_nop 0
	v_mul_f32_e32 v22, 0x4b800000, v21
	v_cmp_gt_f32_e64 s[2:3], s56, v21
	v_cmp_gt_f32_e64 s[0:1], s56, v20
	s_nop 0
	v_cndmask_b32_e64 v21, v21, v22, s[2:3]
	v_rsq_f32_e32 v21, v21
	s_nop 0
	v_mul_f32_e32 v22, 0x45800000, v21
	v_cndmask_b32_e64 v22, v21, v22, s[2:3]
	v_pk_mul_f32 v[18:19], v[18:19], v[22:23] op_sel_hi:[1,0]
	v_pk_mul_f32 v[2:3], v[2:3], v[22:23] op_sel_hi:[1,0]
	v_pk_fma_f32 v[4:5], v[4:5], v[18:19], v[8:9]
	v_pk_fma_f32 v[2:3], v[6:7], v[2:3], v[10:11]
	v_mul_f32_e32 v6, 0xbfb8aa3b, v4
	v_mul_f32_e32 v7, 0xbfb8aa3b, v5
	v_exp_f32_e32 v6, v6
	v_exp_f32_e32 v7, v7
	v_add_f32_e32 v6, 1.0, v6
	v_add_f32_e32 v7, 1.0, v7
	v_rcp_f32_e32 v6, v6
	v_rcp_f32_e32 v7, v7
	s_nop 0
	v_pk_mul_f32 v[4:5], v[4:5], v[6:7]
	s_nop 0
	v_cvt_pk_bf16_f32 v4, v4, v5
	v_mul_f32_e32 v5, 0xbfb8aa3b, v2
	v_exp_f32_e32 v5, v5
	s_nop 0
	v_add_f32_e32 v5, 1.0, v5
	v_rcp_f32_e32 v6, v5
	v_mul_f32_e32 v5, 0xbfb8aa3b, v3
	v_exp_f32_e32 v5, v5
	s_nop 0
	v_add_f32_e32 v5, 1.0, v5
	v_rcp_f32_e32 v7, v5
	s_nop 0
	v_pk_mul_f32 v[2:3], v[2:3], v[6:7]
	s_nop 0
	v_cvt_pk_bf16_f32 v5, v2, v3
	global_store_dwordx2 v[0:1], v[4:5], off
	v_mul_f32_e32 v0, 0x4b800000, v20
	v_cndmask_b32_e64 v0, v20, v0, s[0:1]
	v_rsq_f32_e32 v0, v0
	s_nop 0
	v_mul_f32_e32 v1, 0x45800000, v0
	v_cndmask_b32_e64 v8, v0, v1, s[0:1]
	v_mov_b64_e32 v[0:1], v[172:173]
	v_mov_b64_e32 v[2:3], v[174:175]
	v_mov_b64_e32 v[4:5], v[176:177]
	v_mov_b64_e32 v[6:7], v[178:179]
	v_pk_mul_f32 v[10:11], v[12:13], v[8:9] op_sel_hi:[1,0]
	v_pk_mul_f32 v[8:9], v[14:15], v[8:9] op_sel_hi:[1,0]
	s_add_u32 s0, s4, s28
	s_addc_u32 s1, s5, s30
	s_lshl_b64 s[0:1], s[0:1], 11
	v_add_u32_e32 v12, s47, v105
	v_pk_fma_f32 v[0:1], v[0:1], v[10:11], v[4:5]
	s_nop 0
	v_mul_f32_e32 v4, 0xbfb8aa3b, v0
	v_mul_f32_e32 v5, 0xbfb8aa3b, v1
	v_exp_f32_e32 v4, v4
	v_exp_f32_e32 v5, v5
	v_pk_fma_f32 v[2:3], v[2:3], v[8:9], v[6:7]
	v_add_f32_e32 v4, 1.0, v4
	v_add_f32_e32 v5, 1.0, v5
	v_rcp_f32_e32 v4, v4
	v_rcp_f32_e32 v5, v5
	s_nop 0
	v_pk_mul_f32 v[0:1], v[0:1], v[4:5]
	s_nop 0
	v_cvt_pk_bf16_f32 v0, v0, v1
	v_mul_f32_e32 v1, 0xbfb8aa3b, v2
	v_exp_f32_e32 v1, v1
	s_nop 0
	v_add_f32_e32 v1, 1.0, v1
	v_rcp_f32_e32 v4, v1
	v_mul_f32_e32 v1, 0xbfb8aa3b, v3
	v_exp_f32_e32 v1, v1
	s_nop 0
	v_add_f32_e32 v1, 1.0, v1
	v_rcp_f32_e32 v5, v1
	s_nop 0
	v_pk_mul_f32 v[2:3], v[2:3], v[4:5]
	s_nop 0
	v_cvt_pk_bf16_f32 v1, v2, v3
	v_lshl_add_u64 v[2:3], v[60:61], 0, s[0:1]
	global_store_dwordx2 v[2:3], v[0:1], off
	v_add_u32_e32 v0, s34, v105
	ds_read_b128 v[0:3], v0
	s_add_u32 s0, s4, s31
	s_addc_u32 s1, s5, s35
	s_lshl_b64 s[0:1], s[0:1], 11
	s_waitcnt lgkmcnt(0)
	v_add_f32_e32 v4, v0, v1
	v_add_f32_e32 v4, v2, v4
	v_add_f32_e32 v4, v3, v4
	ds_swizzle_b32 v5, v4 offset:swizzle(SWAP,1)
	s_waitcnt lgkmcnt(0)
	v_add_f32_e32 v4, v4, v5
	ds_swizzle_b32 v5, v4 offset:swizzle(SWAP,2)
	s_waitcnt lgkmcnt(0)
	v_add_f32_e32 v4, v4, v5
	ds_swizzle_b32 v5, v4 offset:swizzle(SWAP,4)
	s_waitcnt lgkmcnt(0)
	v_add_f32_e32 v4, v4, v5
	ds_swizzle_b32 v5, v4 offset:swizzle(SWAP,8)
	s_waitcnt lgkmcnt(0)
	v_add_f32_e32 v4, v4, v5
	ds_swizzle_b32 v5, v4 offset:swizzle(SWAP,16)
	s_waitcnt lgkmcnt(0)
	v_add_f32_e32 v4, v4, v5
	v_mov_b32_e32 v5, v4
	s_nop 1
	v_permlane32_swap_b32_e32 v4, v5
	v_add_f32_e32 v4, v4, v5
	v_fmamk_f32 v19, v4, 0xbb800000, v1
	v_fmamk_f32 v18, v4, 0xbb800000, v0
	v_fmamk_f32 v3, v4, 0xbb800000, v3
	v_fmac_f32_e32 v2, 0xbb800000, v4
	v_pk_mul_f32 v[4:5], v[18:19], v[18:19]
	v_pk_mul_f32 v[0:1], v[2:3], v[2:3]
	v_add_f32_e32 v4, v4, v5
	v_add_f32_e32 v0, v0, v4
	v_mov_b64_e32 v[4:5], v[172:173]
	v_mov_b64_e32 v[6:7], v[174:175]
	v_mov_b64_e32 v[8:9], v[176:177]
	v_mov_b64_e32 v[10:11], v[178:179]
	ds_read_b128 v[12:15], v12
	v_add_f32_e32 v0, v1, v0
	ds_swizzle_b32 v1, v0 offset:swizzle(SWAP,1)
	s_waitcnt lgkmcnt(1)
	v_add_f32_e32 v20, v12, v13
	v_add_f32_e32 v20, v14, v20
	v_add_f32_e32 v20, v15, v20
	ds_swizzle_b32 v22, v20 offset:swizzle(SWAP,1)
	s_waitcnt lgkmcnt(1)
	v_add_f32_e32 v0, v0, v1
	ds_swizzle_b32 v1, v0 offset:swizzle(SWAP,2)
	s_waitcnt lgkmcnt(1)
	v_add_f32_e32 v20, v20, v22
	ds_swizzle_b32 v22, v20 offset:swizzle(SWAP,2)
	s_waitcnt lgkmcnt(1)
	v_add_f32_e32 v0, v0, v1
	ds_swizzle_b32 v1, v0 offset:swizzle(SWAP,4)
	s_waitcnt lgkmcnt(1)
	v_add_f32_e32 v20, v20, v22
	ds_swizzle_b32 v22, v20 offset:swizzle(SWAP,4)
	s_waitcnt lgkmcnt(1)
	v_add_f32_e32 v0, v0, v1
	ds_swizzle_b32 v1, v0 offset:swizzle(SWAP,8)
	s_waitcnt lgkmcnt(1)
	v_add_f32_e32 v20, v20, v22
	ds_swizzle_b32 v22, v20 offset:swizzle(SWAP,8)
	s_waitcnt lgkmcnt(1)
	v_add_f32_e32 v0, v0, v1
	ds_swizzle_b32 v1, v0 offset:swizzle(SWAP,16)
	s_waitcnt lgkmcnt(1)
	v_add_f32_e32 v20, v20, v22
	ds_swizzle_b32 v22, v20 offset:swizzle(SWAP,16)
	s_waitcnt lgkmcnt(1)
	v_add_f32_e32 v21, v0, v1
	v_mov_b32_e32 v23, v21
	s_nop 1
	v_permlane32_swap_b32_e32 v21, v23
	s_waitcnt lgkmcnt(0)
	v_add_f32_e32 v20, v20, v22
	v_mov_b32_e32 v22, v20
	s_nop 1
	v_permlane32_swap_b32_e32 v20, v22
	v_add_f32_e32 v20, v20, v22
	v_fmamk_f32 v13, v20, 0xbb800000, v13
	v_fmamk_f32 v12, v20, 0xbb800000, v12
	v_fmamk_f32 v15, v20, 0xbb800000, v15
	v_fmac_f32_e32 v14, 0xbb800000, v20
	v_pk_mul_f32 v[26:27], v[12:13], v[12:13]
	v_pk_mul_f32 v[24:25], v[14:15], v[14:15]
	v_add_f32_e32 v20, v26, v27
	v_add_f32_e32 v20, v24, v20
	v_add_f32_e32 v20, v25, v20
	ds_swizzle_b32 v22, v20 offset:swizzle(SWAP,1)
	v_lshl_add_u64 v[0:1], v[60:61], 0, s[0:1]
	s_waitcnt lgkmcnt(0)
	v_add_f32_e32 v20, v20, v22
	ds_swizzle_b32 v22, v20 offset:swizzle(SWAP,2)
	s_waitcnt lgkmcnt(0)
	v_add_f32_e32 v20, v20, v22
	ds_swizzle_b32 v22, v20 offset:swizzle(SWAP,4)
	s_waitcnt lgkmcnt(0)
	v_add_f32_e32 v20, v20, v22
	ds_swizzle_b32 v22, v20 offset:swizzle(SWAP,8)
	s_waitcnt lgkmcnt(0)
	v_add_f32_e32 v20, v20, v22
	ds_swizzle_b32 v22, v20 offset:swizzle(SWAP,16)
	s_waitcnt lgkmcnt(0)
	v_add_f32_e32 v20, v20, v22
	v_mov_b32_e32 v22, v20
	s_nop 1
	v_permlane32_swap_b32_e32 v20, v22
	v_pk_add_f32 v[20:21], v[20:21], v[22:23]
	s_nop 0
	v_pk_fma_f32 v[16:17], v[20:21], s[52:53], v[16:17] op_sel_hi:[1,0,0]
	s_nop 0
	v_mul_f32_e32 v20, 0x4b800000, v17
	v_cmp_gt_f32_e64 s[2:3], s56, v17
	v_cmp_gt_f32_e64 s[0:1], s56, v16
	s_nop 0
	v_cndmask_b32_e64 v17, v17, v20, s[2:3]
	v_rsq_f32_e32 v17, v17
	s_nop 0
	v_mul_f32_e32 v20, 0x45800000, v17
	v_cndmask_b32_e64 v20, v17, v20, s[2:3]
	v_pk_mul_f32 v[18:19], v[18:19], v[20:21] op_sel_hi:[1,0]
	v_pk_mul_f32 v[2:3], v[2:3], v[20:21] op_sel_hi:[1,0]
	v_pk_fma_f32 v[4:5], v[4:5], v[18:19], v[8:9]
	v_pk_fma_f32 v[2:3], v[6:7], v[2:3], v[10:11]
	v_mul_f32_e32 v6, 0xbfb8aa3b, v4
	v_mul_f32_e32 v7, 0xbfb8aa3b, v5
	v_exp_f32_e32 v6, v6
	v_exp_f32_e32 v7, v7
	v_add_f32_e32 v6, 1.0, v6
	v_add_f32_e32 v7, 1.0, v7
	v_rcp_f32_e32 v6, v6
	v_rcp_f32_e32 v7, v7
	s_nop 0
	v_pk_mul_f32 v[4:5], v[4:5], v[6:7]
	s_nop 0
	v_cvt_pk_bf16_f32 v4, v4, v5
	v_mul_f32_e32 v5, 0xbfb8aa3b, v2
	v_exp_f32_e32 v5, v5
	s_nop 0
	v_add_f32_e32 v5, 1.0, v5
	v_rcp_f32_e32 v6, v5
	v_mul_f32_e32 v5, 0xbfb8aa3b, v3
	v_exp_f32_e32 v5, v5
	s_nop 0
	v_add_f32_e32 v5, 1.0, v5
	v_rcp_f32_e32 v7, v5
	s_nop 0
	v_pk_mul_f32 v[2:3], v[2:3], v[6:7]
	s_nop 0
	v_cvt_pk_bf16_f32 v5, v2, v3
	global_store_dwordx2 v[0:1], v[4:5], off
	v_mul_f32_e32 v0, 0x4b800000, v16
	v_cndmask_b32_e64 v0, v16, v0, s[0:1]
	v_rsq_f32_e32 v0, v0
	s_nop 0
	v_mul_f32_e32 v1, 0x45800000, v0
	v_cndmask_b32_e64 v8, v0, v1, s[0:1]
	v_mov_b64_e32 v[0:1], v[172:173]
	v_mov_b64_e32 v[2:3], v[174:175]
	v_mov_b64_e32 v[4:5], v[176:177]
	v_mov_b64_e32 v[6:7], v[178:179]
	v_pk_mul_f32 v[10:11], v[12:13], v[8:9] op_sel_hi:[1,0]
	v_pk_mul_f32 v[8:9], v[14:15], v[8:9] op_sel_hi:[1,0]
	s_add_u32 s0, s4, s46
	s_addc_u32 s1, s5, s48
	s_lshl_b64 s[0:1], s[0:1], 11
	s_add_i32 s50, s50, s93
	v_pk_fma_f32 v[0:1], v[0:1], v[10:11], v[4:5]
	s_nop 0
	v_mul_f32_e32 v4, 0xbfb8aa3b, v0
	v_mul_f32_e32 v5, 0xbfb8aa3b, v1
	v_exp_f32_e32 v4, v4
	v_exp_f32_e32 v5, v5
	v_pk_fma_f32 v[2:3], v[2:3], v[8:9], v[6:7]
	v_add_f32_e32 v4, 1.0, v4
	v_add_f32_e32 v5, 1.0, v5
	v_rcp_f32_e32 v4, v4
	v_rcp_f32_e32 v5, v5
	s_nop 0
	v_pk_mul_f32 v[0:1], v[0:1], v[4:5]
	s_nop 0
	v_cvt_pk_bf16_f32 v0, v0, v1
	v_mul_f32_e32 v1, 0xbfb8aa3b, v2
	v_exp_f32_e32 v1, v1
	s_nop 0
	v_add_f32_e32 v1, 1.0, v1
	v_rcp_f32_e32 v4, v1
	v_mul_f32_e32 v1, 0xbfb8aa3b, v3
	v_exp_f32_e32 v1, v1
	s_nop 0
	v_add_f32_e32 v1, 1.0, v1
	v_rcp_f32_e32 v5, v1
	s_nop 0
	v_pk_mul_f32 v[2:3], v[2:3], v[4:5]
	s_nop 0
	v_cvt_pk_bf16_f32 v1, v2, v3
	v_lshl_add_u64 v[2:3], v[60:61], 0, s[0:1]
	v_readlane_b32 s0, v252, 59
	s_add_i32 s49, s49, s0
	s_cmpk_lt_i32 s50, 0x100
	global_store_dwordx2 v[2:3], v[0:1], off
	s_cbranch_scc0 .LBB0_517
